# speedup vs baseline: 1.0014x; 1.0014x over previous
_Z11gemm_kernelILi1EEvPKDF16_S1_iiiPDF16_PfPKfi:
	s_load_dwordx8 s[4:11], s[0:1], 0x0
	s_and_b32 s3, s2, 7
	s_lshl_b32 s3, s3, 3
	s_bfe_u32 s14, s2, 0x30003
	s_add_i32 s3, s3, s14
	s_lshr_b32 s15, s2, 6
	v_lshrrev_b32_e32 v2, 4, v0
	v_xor_b32_e32 v75, v2, v0
	v_lshrrev_b32_e32 v2, 3, v0
	v_lshlrev_b32_e32 v74, 4, v0
	v_bfe_u32 v70, v0, 6, 1
	v_readfirstlane_b32 s20, v74
	s_waitcnt lgkmcnt(0)
	s_mov_b32 s9, s15
	s_mov_b32 s11, s3
	s_mov_b32 s14, 0
	s_mov_b32 s15, 0
	s_mov_b32 s16, 0
	s_mov_b32 s17, 0
	v_mul_lo_u32 v2, v2, s10
	v_lshlrev_b32_e32 v1, 3, v75
	s_lshl_b32 s12, s3, 7
	v_and_b32_e32 v1, 56, v1
	v_add_lshl_u32 v64, v2, v1, 1
	v_bfe_u32 v2, v0, 3, 25
	s_mul_hi_i32 s3, s12, s10
	s_mul_i32 s2, s12, s10
	v_or_b32_e32 v3, 32, v2
	s_lshl_b32 s13, s9, 7
	s_lshl_b64 s[2:3], s[2:3], 1
	v_mul_lo_u32 v3, v3, s10
	s_add_u32 s8, s4, s2
	v_add_lshl_u32 v66, v3, v1, 1
	v_or_b32_e32 v3, 64, v2
	v_or_b32_e32 v2, 0x60, v2
	s_addc_u32 s9, s5, s3
	s_mul_hi_i32 s3, s13, s10
	s_mul_i32 s2, s13, s10
	v_mul_lo_u32 v3, v3, s10
	v_mul_lo_u32 v76, v2, s10
	s_lshl_b64 s[2:3], s[2:3], 1
	v_add_lshl_u32 v68, v3, v1, 1
	v_add_lshl_u32 v2, v76, v1, 1
	s_add_u32 s18, s6, s2
	v_or_b32_e32 v1, 0x4000, v74
	v_ashrrev_i32_e32 v65, 31, v64
	s_addc_u32 s19, s7, s3
	v_lshl_add_u64 v[4:5], s[8:9], 0, v[64:65]
	s_mov_b32 m0, s20
	v_readfirstlane_b32 s20, v1
	v_or_b32_e32 v1, 0x1000, v74
	global_load_lds_dwordx4 v[4:5], off
	v_lshl_add_u64 v[4:5], s[18:19], 0, v[64:65]
	s_mov_b32 m0, s20
	v_ashrrev_i32_e32 v67, 31, v66
	v_readfirstlane_b32 s20, v1
	v_or_b32_e32 v1, 0x5000, v74
	global_load_lds_dwordx4 v[4:5], off
	v_lshl_add_u64 v[4:5], s[8:9], 0, v[66:67]
	s_mov_b32 m0, s20
	v_readfirstlane_b32 s20, v1
	v_or_b32_e32 v1, 0x2000, v74
	global_load_lds_dwordx4 v[4:5], off
	v_lshl_add_u64 v[4:5], s[18:19], 0, v[66:67]
	s_mov_b32 m0, s20
	v_ashrrev_i32_e32 v69, 31, v68
	v_readfirstlane_b32 s20, v1
	v_or_b32_e32 v1, 0x6000, v74
	global_load_lds_dwordx4 v[4:5], off
	v_lshl_add_u64 v[4:5], s[8:9], 0, v[68:69]
	s_mov_b32 m0, s20
	v_readfirstlane_b32 s20, v1
	global_load_lds_dwordx4 v[4:5], off
	v_lshl_add_u64 v[4:5], s[18:19], 0, v[68:69]
	s_mov_b32 m0, s20
	v_ashrrev_i32_e32 v3, 31, v2
	v_or_b32_e32 v1, 0x3000, v74
	global_load_lds_dwordx4 v[4:5], off
	v_lshl_add_u64 v[4:5], s[8:9], 0, v[2:3]
	v_readfirstlane_b32 s8, v1
	v_or_b32_e32 v1, 0x7000, v74
	s_mov_b32 m0, s8
	v_readfirstlane_b32 s8, v1
	global_load_lds_dwordx4 v[4:5], off
	v_lshl_add_u64 v[2:3], s[18:19], 0, v[2:3]
	s_mov_b32 m0, s8
	s_mov_b32 s8, 0
	global_load_lds_dwordx4 v[2:3], off
	v_lshrrev_b32_e32 v73, 7, v0
	v_bfe_u32 v71, v0, 4, 2
	v_and_b32_e32 v72, 15, v0
	v_mov_b32_e32 v3, 0
	s_cmp_lt_i32 s10, 64
	v_mov_b32_e32 v2, 0
	v_mov_b32_e32 v1, 0
	v_mov_b32_e32 v0, 0
	v_mov_b32_e32 v7, 0
	v_mov_b32_e32 v6, 0
	v_mov_b32_e32 v5, 0
	v_mov_b32_e32 v4, 0
	v_mov_b32_e32 v11, 0
	v_mov_b32_e32 v10, 0
	v_mov_b32_e32 v9, 0
	v_mov_b32_e32 v8, 0
	v_mov_b32_e32 v15, 0
	v_mov_b32_e32 v14, 0
	v_mov_b32_e32 v13, 0
	v_mov_b32_e32 v12, 0
	v_mov_b32_e32 v63, 0
	v_mov_b32_e32 v62, 0
	v_mov_b32_e32 v61, 0
	v_mov_b32_e32 v60, 0
	v_mov_b32_e32 v59, 0
	v_mov_b32_e32 v58, 0
	v_mov_b32_e32 v57, 0
	v_mov_b32_e32 v56, 0
	v_mov_b32_e32 v55, 0
	v_mov_b32_e32 v54, 0
	v_mov_b32_e32 v53, 0
	v_mov_b32_e32 v52, 0
	v_mov_b32_e32 v51, 0
	v_mov_b32_e32 v50, 0
	v_mov_b32_e32 v49, 0
	v_mov_b32_e32 v48, 0
	v_mov_b32_e32 v47, 0
	v_mov_b32_e32 v46, 0
	v_mov_b32_e32 v45, 0
	v_mov_b32_e32 v44, 0
	v_mov_b32_e32 v43, 0
	v_mov_b32_e32 v42, 0
	v_mov_b32_e32 v41, 0
	v_mov_b32_e32 v40, 0
	v_mov_b32_e32 v39, 0
	v_mov_b32_e32 v38, 0
	v_mov_b32_e32 v37, 0
	v_mov_b32_e32 v36, 0
	v_mov_b32_e32 v35, 0
	v_mov_b32_e32 v34, 0
	v_mov_b32_e32 v33, 0
	v_mov_b32_e32 v32, 0
	v_mov_b32_e32 v31, 0
	v_mov_b32_e32 v30, 0
	v_mov_b32_e32 v29, 0
	v_mov_b32_e32 v28, 0
	v_mov_b32_e32 v27, 0
	v_mov_b32_e32 v26, 0
	v_mov_b32_e32 v25, 0
	v_mov_b32_e32 v24, 0
	v_mov_b32_e32 v23, 0
	v_mov_b32_e32 v22, 0
	v_mov_b32_e32 v21, 0
	v_mov_b32_e32 v20, 0
	v_mov_b32_e32 v19, 0
	v_mov_b32_e32 v18, 0
	v_mov_b32_e32 v17, 0
	v_mov_b32_e32 v16, 0
	s_cbranch_scc1 .LBB8_10
	s_lshl_b32 s15, s15, 3
	s_add_i32 s11, s11, s15
	s_sub_i32 s11, s11, s17
	s_sub_i32 s11, s11, s16
	s_lshl_b32 s14, s14, 3
	s_ashr_i32 s9, s10, 31
	s_sub_i32 s11, s11, s14
	v_lshrrev_b32_e32 v1, 1, v72
	s_lshr_b32 s9, s9, 26
	s_lshl_b32 s14, s11, 7
	v_lshlrev_b32_e32 v0, 7, v72
	v_xor_b32_e32 v1, v71, v1
	s_add_i32 s9, s10, s9
	s_mul_hi_i32 s11, s10, s14
	s_mul_i32 s10, s10, s14
	v_lshl_or_b32 v0, v1, 4, v0
	v_lshlrev_b32_e32 v1, 13, v73
	v_lshlrev_b32_e32 v2, 13, v70
	s_ashr_i32 s9, s9, 6
	s_lshl_b64 s[10:11], s[10:11], 1
	v_or_b32_e32 v16, v0, v2
	v_or_b32_e32 v17, v0, v1
	v_bitop3_b32 v18, v0, 64, v1 bitop3:0x36
	v_bitop3_b32 v19, v0, 64, v2 bitop3:0x36
	v_and_b32_e32 v0, 7, v75
	s_add_u32 s4, s4, s10
	v_lshlrev_b32_e32 v0, 4, v0
	s_addc_u32 s5, s5, s11
	v_lshl_add_u32 v8, v76, 1, v0
	s_add_u32 s2, s6, s2
	v_ashrrev_i32_e32 v9, 31, v8
	s_addc_u32 s3, s7, s3
	v_lshl_add_u64 v[0:1], s[4:5], 0, v[8:9]
	s_mov_b64 s[10:11], 0x80
	v_lshl_add_u64 v[2:3], s[4:5], 0, v[68:69]
	v_lshl_add_u64 v[4:5], s[4:5], 0, v[66:67]
	v_lshl_add_u64 v[6:7], s[4:5], 0, v[64:65]
	v_lshl_add_u64 v[8:9], s[2:3], 0, v[8:9]
	v_lshl_add_u64 v[10:11], s[2:3], 0, v[68:69]
	v_lshl_add_u64 v[12:13], s[2:3], 0, v[66:67]
	v_lshl_add_u64 v[14:15], s[2:3], 0, v[64:65]
	v_lshl_add_u64 v[0:1], v[0:1], 0, s[10:11]
	v_lshl_add_u64 v[2:3], v[2:3], 0, s[10:11]
	v_lshl_add_u64 v[4:5], v[4:5], 0, s[10:11]
	v_lshl_add_u64 v[6:7], v[6:7], 0, s[10:11]
	v_lshl_add_u64 v[8:9], v[8:9], 0, s[10:11]
	v_lshl_add_u64 v[10:11], v[10:11], 0, s[10:11]
	v_lshl_add_u64 v[12:13], v[12:13], 0, s[10:11]
	v_lshl_add_u64 v[14:15], v[14:15], 0, s[10:11]
	v_accvgpr_write_b32 a63, 0
	v_accvgpr_write_b32 a62, 0
	v_accvgpr_write_b32 a61, 0
	v_accvgpr_write_b32 a60, 0
	v_accvgpr_write_b32 a59, 0
	v_accvgpr_write_b32 a58, 0
	v_accvgpr_write_b32 a57, 0
	v_accvgpr_write_b32 a56, 0
	v_accvgpr_write_b32 a55, 0
	v_accvgpr_write_b32 a54, 0
	v_accvgpr_write_b32 a53, 0
	v_accvgpr_write_b32 a52, 0
	v_accvgpr_write_b32 a51, 0
	v_accvgpr_write_b32 a50, 0
	v_accvgpr_write_b32 a49, 0
	v_accvgpr_write_b32 a48, 0
	v_accvgpr_write_b32 a3, 0
	v_accvgpr_write_b32 a2, 0
	v_accvgpr_write_b32 a1, 0
	v_accvgpr_write_b32 a0, 0
	v_accvgpr_write_b32 a7, 0
	v_accvgpr_write_b32 a6, 0
	v_accvgpr_write_b32 a5, 0
	v_accvgpr_write_b32 a4, 0
	v_accvgpr_write_b32 a11, 0
	v_accvgpr_write_b32 a10, 0
	v_accvgpr_write_b32 a9, 0
	v_accvgpr_write_b32 a8, 0
	v_accvgpr_write_b32 a15, 0
	v_accvgpr_write_b32 a14, 0
	v_accvgpr_write_b32 a13, 0
	v_accvgpr_write_b32 a12, 0
	v_accvgpr_write_b32 a19, 0
	v_accvgpr_write_b32 a18, 0
	v_accvgpr_write_b32 a17, 0
	v_accvgpr_write_b32 a16, 0
	v_accvgpr_write_b32 a23, 0
	v_accvgpr_write_b32 a22, 0
	v_accvgpr_write_b32 a21, 0
	v_accvgpr_write_b32 a20, 0
	v_accvgpr_write_b32 a27, 0
	v_accvgpr_write_b32 a26, 0
	v_accvgpr_write_b32 a25, 0
	v_accvgpr_write_b32 a24, 0
	v_accvgpr_write_b32 a31, 0
	v_accvgpr_write_b32 a30, 0
	v_accvgpr_write_b32 a29, 0
	v_accvgpr_write_b32 a28, 0
	v_accvgpr_write_b32 a35, 0
	v_accvgpr_write_b32 a34, 0
	v_accvgpr_write_b32 a33, 0
	v_accvgpr_write_b32 a32, 0
	v_accvgpr_write_b32 a39, 0
	v_accvgpr_write_b32 a38, 0
	v_accvgpr_write_b32 a37, 0
	v_accvgpr_write_b32 a36, 0
	v_accvgpr_write_b32 a43, 0
	v_accvgpr_write_b32 a42, 0
	v_accvgpr_write_b32 a41, 0
	v_accvgpr_write_b32 a40, 0
	v_accvgpr_write_b32 a47, 0
	v_accvgpr_write_b32 a46, 0
	v_accvgpr_write_b32 a45, 0
	v_accvgpr_write_b32 a44, 0
	v_readfirstlane_b32 s20, v74
	v_add_u32_e32 v22, 0x10000, v16
	v_add_u32_e32 v23, 0x10000, v17
	v_add_u32_e32 v24, 0x10000, v18
	v_add_u32_e32 v25, 0x10000, v19
	s_mov_b64 s[2:3], 0x0
	s_add_u32 m0, s20, 0x8000
	v_lshl_add_u64 v[20:21], v[6:7], 0, s[2:3]
	global_load_lds_dwordx4 v[20:21], off
	s_add_u32 m0, s20, 0xc000
	v_lshl_add_u64 v[20:21], v[14:15], 0, s[2:3]
	global_load_lds_dwordx4 v[20:21], off
	s_add_u32 m0, s20, 0x9000
	v_lshl_add_u64 v[20:21], v[4:5], 0, s[2:3]
	global_load_lds_dwordx4 v[20:21], off
	s_add_u32 m0, s20, 0xd000
	v_lshl_add_u64 v[20:21], v[12:13], 0, s[2:3]
	global_load_lds_dwordx4 v[20:21], off
	s_add_u32 m0, s20, 0xa000
	v_lshl_add_u64 v[20:21], v[2:3], 0, s[2:3]
	global_load_lds_dwordx4 v[20:21], off
	s_add_u32 m0, s20, 0xe000
	v_lshl_add_u64 v[20:21], v[10:11], 0, s[2:3]
	global_load_lds_dwordx4 v[20:21], off
	s_add_u32 m0, s20, 0xb000
	v_lshl_add_u64 v[20:21], v[0:1], 0, s[2:3]
	global_load_lds_dwordx4 v[20:21], off
	s_add_u32 m0, s20, 0xf000
	v_lshl_add_u64 v[20:21], v[8:9], 0, s[2:3]
	global_load_lds_dwordx4 v[20:21], off
	s_mov_b64 s[2:3], 0x80
	s_add_u32 m0, s20, 0x10000
	v_lshl_add_u64 v[20:21], v[6:7], 0, s[2:3]
	global_load_lds_dwordx4 v[20:21], off
	s_add_u32 m0, s20, 0x14000
	v_lshl_add_u64 v[20:21], v[14:15], 0, s[2:3]
	global_load_lds_dwordx4 v[20:21], off
	s_add_u32 m0, s20, 0x11000
	v_lshl_add_u64 v[20:21], v[4:5], 0, s[2:3]
	global_load_lds_dwordx4 v[20:21], off
	s_add_u32 m0, s20, 0x15000
	v_lshl_add_u64 v[20:21], v[12:13], 0, s[2:3]
	global_load_lds_dwordx4 v[20:21], off
	s_add_u32 m0, s20, 0x12000
	v_lshl_add_u64 v[20:21], v[2:3], 0, s[2:3]
	global_load_lds_dwordx4 v[20:21], off
	s_add_u32 m0, s20, 0x16000
	v_lshl_add_u64 v[20:21], v[10:11], 0, s[2:3]
	global_load_lds_dwordx4 v[20:21], off
	s_add_u32 m0, s20, 0x13000
	v_lshl_add_u64 v[20:21], v[0:1], 0, s[2:3]
	global_load_lds_dwordx4 v[20:21], off
	s_add_u32 m0, s20, 0x17000
	v_lshl_add_u64 v[20:21], v[8:9], 0, s[2:3]
	global_load_lds_dwordx4 v[20:21], off
	s_waitcnt vmcnt(16)
	s_barrier
	ds_read_b128 v[80:83], v17
	ds_read_b128 v[96:99], v16 offset:16384
	ds_read_b128 v[84:87], v17 offset:2048
	ds_read_b128 v[100:103], v16 offset:18432
	ds_read_b128 v[88:91], v17 offset:4096
	ds_read_b128 v[104:107], v16 offset:20480
	ds_read_b128 v[92:95], v17 offset:6144
	ds_read_b128 v[108:111], v16 offset:22528
	s_waitcnt lgkmcnt(0)
	v_mfma_f32_16x16x32_f16 a[0:3], v[96:99], v[80:83], a[0:3]
	ds_read_b128 v[112:115], v18
	v_mfma_f32_16x16x32_f16 a[4:7], v[100:103], v[80:83], a[4:7]
	ds_read_b128 v[128:131], v19 offset:16384
	v_mfma_f32_16x16x32_f16 a[8:11], v[104:107], v[80:83], a[8:11]
	ds_read_b128 v[116:119], v18 offset:2048
	v_mfma_f32_16x16x32_f16 a[12:15], v[108:111], v[80:83], a[12:15]
	ds_read_b128 v[132:135], v19 offset:18432
	v_mfma_f32_16x16x32_f16 a[16:19], v[96:99], v[84:87], a[16:19]
	ds_read_b128 v[120:123], v18 offset:4096
	v_mfma_f32_16x16x32_f16 a[20:23], v[100:103], v[84:87], a[20:23]
	ds_read_b128 v[136:139], v19 offset:20480
	v_mfma_f32_16x16x32_f16 a[24:27], v[104:107], v[84:87], a[24:27]
	ds_read_b128 v[124:127], v18 offset:6144
	v_mfma_f32_16x16x32_f16 a[28:31], v[108:111], v[84:87], a[28:31]
	ds_read_b128 v[140:143], v19 offset:22528
	v_mfma_f32_16x16x32_f16 a[32:35], v[96:99], v[88:91], a[32:35]
	v_mfma_f32_16x16x32_f16 a[36:39], v[100:103], v[88:91], a[36:39]
	v_mfma_f32_16x16x32_f16 a[40:43], v[104:107], v[88:91], a[40:43]
	v_mfma_f32_16x16x32_f16 a[44:47], v[108:111], v[88:91], a[44:47]
	v_mfma_f32_16x16x32_f16 a[48:51], v[96:99], v[92:95], a[48:51]
	v_mfma_f32_16x16x32_f16 a[52:55], v[100:103], v[92:95], a[52:55]
	v_mfma_f32_16x16x32_f16 a[56:59], v[104:107], v[92:95], a[56:59]
	v_mfma_f32_16x16x32_f16 a[60:63], v[108:111], v[92:95], a[60:63]
	s_waitcnt vmcnt(8)
	s_barrier
	s_mov_b64 s[2:3], 0x100
	s_waitcnt lgkmcnt(0)
	v_mfma_f32_16x16x32_f16 a[0:3], v[128:131], v[112:115], a[0:3]
	ds_read_b128 v[80:83], v17 offset:32768
	v_mfma_f32_16x16x32_f16 a[4:7], v[132:135], v[112:115], a[4:7]
	ds_read_b128 v[96:99], v16 offset:49152
	v_mfma_f32_16x16x32_f16 a[8:11], v[136:139], v[112:115], a[8:11]
	ds_read_b128 v[84:87], v17 offset:34816
	v_mfma_f32_16x16x32_f16 a[12:15], v[140:143], v[112:115], a[12:15]
	ds_read_b128 v[100:103], v16 offset:51200
	v_mfma_f32_16x16x32_f16 a[16:19], v[128:131], v[116:119], a[16:19]
	ds_read_b128 v[88:91], v17 offset:36864
	v_mfma_f32_16x16x32_f16 a[20:23], v[132:135], v[116:119], a[20:23]
	ds_read_b128 v[104:107], v16 offset:53248
	v_mfma_f32_16x16x32_f16 a[24:27], v[136:139], v[116:119], a[24:27]
	ds_read_b128 v[92:95], v17 offset:38912
	v_mfma_f32_16x16x32_f16 a[28:31], v[140:143], v[116:119], a[28:31]
	ds_read_b128 v[108:111], v16 offset:55296
	v_mfma_f32_16x16x32_f16 a[32:35], v[128:131], v[120:123], a[32:35]
	s_add_u32 m0, s20, 0x18000
	v_lshl_add_u64 v[20:21], v[6:7], 0, s[2:3]
	global_load_lds_dwordx4 v[20:21], off
	v_mfma_f32_16x16x32_f16 a[36:39], v[132:135], v[120:123], a[36:39]
	s_add_u32 m0, s20, 0x1c000
	v_lshl_add_u64 v[20:21], v[14:15], 0, s[2:3]
	global_load_lds_dwordx4 v[20:21], off
	v_mfma_f32_16x16x32_f16 a[40:43], v[136:139], v[120:123], a[40:43]
	s_add_u32 m0, s20, 0x19000
	v_lshl_add_u64 v[20:21], v[4:5], 0, s[2:3]
	global_load_lds_dwordx4 v[20:21], off
	v_mfma_f32_16x16x32_f16 a[44:47], v[140:143], v[120:123], a[44:47]
	s_add_u32 m0, s20, 0x1d000
	v_lshl_add_u64 v[20:21], v[12:13], 0, s[2:3]
	global_load_lds_dwordx4 v[20:21], off
	v_mfma_f32_16x16x32_f16 a[48:51], v[128:131], v[124:127], a[48:51]
	s_add_u32 m0, s20, 0x1a000
	v_lshl_add_u64 v[20:21], v[2:3], 0, s[2:3]
	global_load_lds_dwordx4 v[20:21], off
	v_mfma_f32_16x16x32_f16 a[52:55], v[132:135], v[124:127], a[52:55]
	s_add_u32 m0, s20, 0x1e000
	v_lshl_add_u64 v[20:21], v[10:11], 0, s[2:3]
	global_load_lds_dwordx4 v[20:21], off
	v_mfma_f32_16x16x32_f16 a[56:59], v[136:139], v[124:127], a[56:59]
	s_add_u32 m0, s20, 0x1b000
	v_lshl_add_u64 v[20:21], v[0:1], 0, s[2:3]
	global_load_lds_dwordx4 v[20:21], off
	v_mfma_f32_16x16x32_f16 a[60:63], v[140:143], v[124:127], a[60:63]
	s_add_u32 m0, s20, 0x1f000
	v_lshl_add_u64 v[20:21], v[8:9], 0, s[2:3]
	global_load_lds_dwordx4 v[20:21], off
	s_waitcnt lgkmcnt(0)
	v_mfma_f32_16x16x32_f16 a[0:3], v[96:99], v[80:83], a[0:3]
	ds_read_b128 v[112:115], v18 offset:32768
	v_mfma_f32_16x16x32_f16 a[4:7], v[100:103], v[80:83], a[4:7]
	ds_read_b128 v[128:131], v19 offset:49152
	v_mfma_f32_16x16x32_f16 a[8:11], v[104:107], v[80:83], a[8:11]
	ds_read_b128 v[116:119], v18 offset:34816
	v_mfma_f32_16x16x32_f16 a[12:15], v[108:111], v[80:83], a[12:15]
	ds_read_b128 v[132:135], v19 offset:51200
	v_mfma_f32_16x16x32_f16 a[16:19], v[96:99], v[84:87], a[16:19]
	ds_read_b128 v[120:123], v18 offset:36864
	v_mfma_f32_16x16x32_f16 a[20:23], v[100:103], v[84:87], a[20:23]
	ds_read_b128 v[136:139], v19 offset:53248
	v_mfma_f32_16x16x32_f16 a[24:27], v[104:107], v[84:87], a[24:27]
	ds_read_b128 v[124:127], v18 offset:38912
	v_mfma_f32_16x16x32_f16 a[28:31], v[108:111], v[84:87], a[28:31]
	ds_read_b128 v[140:143], v19 offset:55296
	v_mfma_f32_16x16x32_f16 a[32:35], v[96:99], v[88:91], a[32:35]
	v_mfma_f32_16x16x32_f16 a[36:39], v[100:103], v[88:91], a[36:39]
	v_mfma_f32_16x16x32_f16 a[40:43], v[104:107], v[88:91], a[40:43]
	v_mfma_f32_16x16x32_f16 a[44:47], v[108:111], v[88:91], a[44:47]
	v_mfma_f32_16x16x32_f16 a[48:51], v[96:99], v[92:95], a[48:51]
	v_mfma_f32_16x16x32_f16 a[52:55], v[100:103], v[92:95], a[52:55]
	v_mfma_f32_16x16x32_f16 a[56:59], v[104:107], v[92:95], a[56:59]
	v_mfma_f32_16x16x32_f16 a[60:63], v[108:111], v[92:95], a[60:63]
	s_waitcnt vmcnt(8)
	s_barrier
	s_mov_b64 s[2:3], 0x180
	s_waitcnt lgkmcnt(0)
	v_mfma_f32_16x16x32_f16 a[0:3], v[128:131], v[112:115], a[0:3]
	ds_read_b128 v[80:83], v23
	v_mfma_f32_16x16x32_f16 a[4:7], v[132:135], v[112:115], a[4:7]
	ds_read_b128 v[96:99], v22 offset:16384
	v_mfma_f32_16x16x32_f16 a[8:11], v[136:139], v[112:115], a[8:11]
	ds_read_b128 v[84:87], v23 offset:2048
	v_mfma_f32_16x16x32_f16 a[12:15], v[140:143], v[112:115], a[12:15]
	ds_read_b128 v[100:103], v22 offset:18432
	v_mfma_f32_16x16x32_f16 a[16:19], v[128:131], v[116:119], a[16:19]
	ds_read_b128 v[88:91], v23 offset:4096
	v_mfma_f32_16x16x32_f16 a[20:23], v[132:135], v[116:119], a[20:23]
	ds_read_b128 v[104:107], v22 offset:20480
	v_mfma_f32_16x16x32_f16 a[24:27], v[136:139], v[116:119], a[24:27]
	ds_read_b128 v[92:95], v23 offset:6144
	v_mfma_f32_16x16x32_f16 a[28:31], v[140:143], v[116:119], a[28:31]
	ds_read_b128 v[108:111], v22 offset:22528
	v_mfma_f32_16x16x32_f16 a[32:35], v[128:131], v[120:123], a[32:35]
	s_add_u32 m0, s20, 0x0
	v_lshl_add_u64 v[20:21], v[6:7], 0, s[2:3]
	global_load_lds_dwordx4 v[20:21], off
	v_mfma_f32_16x16x32_f16 a[36:39], v[132:135], v[120:123], a[36:39]
	s_add_u32 m0, s20, 0x4000
	v_lshl_add_u64 v[20:21], v[14:15], 0, s[2:3]
	global_load_lds_dwordx4 v[20:21], off
	v_mfma_f32_16x16x32_f16 a[40:43], v[136:139], v[120:123], a[40:43]
	s_add_u32 m0, s20, 0x1000
	v_lshl_add_u64 v[20:21], v[4:5], 0, s[2:3]
	global_load_lds_dwordx4 v[20:21], off
	v_mfma_f32_16x16x32_f16 a[44:47], v[140:143], v[120:123], a[44:47]
	s_add_u32 m0, s20, 0x5000
	v_lshl_add_u64 v[20:21], v[12:13], 0, s[2:3]
	global_load_lds_dwordx4 v[20:21], off
	v_mfma_f32_16x16x32_f16 a[48:51], v[128:131], v[124:127], a[48:51]
	s_add_u32 m0, s20, 0x2000
	v_lshl_add_u64 v[20:21], v[2:3], 0, s[2:3]
	global_load_lds_dwordx4 v[20:21], off
	v_mfma_f32_16x16x32_f16 a[52:55], v[132:135], v[124:127], a[52:55]
	s_add_u32 m0, s20, 0x6000
	v_lshl_add_u64 v[20:21], v[10:11], 0, s[2:3]
	global_load_lds_dwordx4 v[20:21], off
	v_mfma_f32_16x16x32_f16 a[56:59], v[136:139], v[124:127], a[56:59]
	s_add_u32 m0, s20, 0x3000
	v_lshl_add_u64 v[20:21], v[0:1], 0, s[2:3]
	global_load_lds_dwordx4 v[20:21], off
	v_mfma_f32_16x16x32_f16 a[60:63], v[140:143], v[124:127], a[60:63]
	s_add_u32 m0, s20, 0x7000
	v_lshl_add_u64 v[20:21], v[8:9], 0, s[2:3]
	global_load_lds_dwordx4 v[20:21], off
	s_waitcnt lgkmcnt(0)
	v_mfma_f32_16x16x32_f16 a[0:3], v[96:99], v[80:83], a[0:3]
	ds_read_b128 v[112:115], v24
	v_mfma_f32_16x16x32_f16 a[4:7], v[100:103], v[80:83], a[4:7]
	ds_read_b128 v[128:131], v25 offset:16384
	v_mfma_f32_16x16x32_f16 a[8:11], v[104:107], v[80:83], a[8:11]
	ds_read_b128 v[116:119], v24 offset:2048
	v_mfma_f32_16x16x32_f16 a[12:15], v[108:111], v[80:83], a[12:15]
	ds_read_b128 v[132:135], v25 offset:18432
	v_mfma_f32_16x16x32_f16 a[16:19], v[96:99], v[84:87], a[16:19]
	ds_read_b128 v[120:123], v24 offset:4096
	v_mfma_f32_16x16x32_f16 a[20:23], v[100:103], v[84:87], a[20:23]
	ds_read_b128 v[136:139], v25 offset:20480
	v_mfma_f32_16x16x32_f16 a[24:27], v[104:107], v[84:87], a[24:27]
	ds_read_b128 v[124:127], v24 offset:6144
	v_mfma_f32_16x16x32_f16 a[28:31], v[108:111], v[84:87], a[28:31]
	ds_read_b128 v[140:143], v25 offset:22528
	v_mfma_f32_16x16x32_f16 a[32:35], v[96:99], v[88:91], a[32:35]
	v_mfma_f32_16x16x32_f16 a[36:39], v[100:103], v[88:91], a[36:39]
	v_mfma_f32_16x16x32_f16 a[40:43], v[104:107], v[88:91], a[40:43]
	v_mfma_f32_16x16x32_f16 a[44:47], v[108:111], v[88:91], a[44:47]
	v_mfma_f32_16x16x32_f16 a[48:51], v[96:99], v[92:95], a[48:51]
	v_mfma_f32_16x16x32_f16 a[52:55], v[100:103], v[92:95], a[52:55]
	v_mfma_f32_16x16x32_f16 a[56:59], v[104:107], v[92:95], a[56:59]
	v_mfma_f32_16x16x32_f16 a[60:63], v[108:111], v[92:95], a[60:63]
	s_waitcnt vmcnt(8)
	s_barrier
	s_mov_b64 s[2:3], 0x200
	s_waitcnt lgkmcnt(0)
	v_mfma_f32_16x16x32_f16 a[0:3], v[128:131], v[112:115], a[0:3]
	ds_read_b128 v[80:83], v23 offset:32768
	v_mfma_f32_16x16x32_f16 a[4:7], v[132:135], v[112:115], a[4:7]
	ds_read_b128 v[96:99], v22 offset:49152
	v_mfma_f32_16x16x32_f16 a[8:11], v[136:139], v[112:115], a[8:11]
	ds_read_b128 v[84:87], v23 offset:34816
	v_mfma_f32_16x16x32_f16 a[12:15], v[140:143], v[112:115], a[12:15]
	ds_read_b128 v[100:103], v22 offset:51200
	v_mfma_f32_16x16x32_f16 a[16:19], v[128:131], v[116:119], a[16:19]
	ds_read_b128 v[88:91], v23 offset:36864
	v_mfma_f32_16x16x32_f16 a[20:23], v[132:135], v[116:119], a[20:23]
	ds_read_b128 v[104:107], v22 offset:53248
	v_mfma_f32_16x16x32_f16 a[24:27], v[136:139], v[116:119], a[24:27]
	ds_read_b128 v[92:95], v23 offset:38912
	v_mfma_f32_16x16x32_f16 a[28:31], v[140:143], v[116:119], a[28:31]
	ds_read_b128 v[108:111], v22 offset:55296
	v_mfma_f32_16x16x32_f16 a[32:35], v[128:131], v[120:123], a[32:35]
	s_add_u32 m0, s20, 0x8000
	v_lshl_add_u64 v[20:21], v[6:7], 0, s[2:3]
	global_load_lds_dwordx4 v[20:21], off
	v_mfma_f32_16x16x32_f16 a[36:39], v[132:135], v[120:123], a[36:39]
	s_add_u32 m0, s20, 0xc000
	v_lshl_add_u64 v[20:21], v[14:15], 0, s[2:3]
	global_load_lds_dwordx4 v[20:21], off
	v_mfma_f32_16x16x32_f16 a[40:43], v[136:139], v[120:123], a[40:43]
	s_add_u32 m0, s20, 0x9000
	v_lshl_add_u64 v[20:21], v[4:5], 0, s[2:3]
	global_load_lds_dwordx4 v[20:21], off
	v_mfma_f32_16x16x32_f16 a[44:47], v[140:143], v[120:123], a[44:47]
	s_add_u32 m0, s20, 0xd000
	v_lshl_add_u64 v[20:21], v[12:13], 0, s[2:3]
	global_load_lds_dwordx4 v[20:21], off
	v_mfma_f32_16x16x32_f16 a[48:51], v[128:131], v[124:127], a[48:51]
	s_add_u32 m0, s20, 0xa000
	v_lshl_add_u64 v[20:21], v[2:3], 0, s[2:3]
	global_load_lds_dwordx4 v[20:21], off
	v_mfma_f32_16x16x32_f16 a[52:55], v[132:135], v[124:127], a[52:55]
	s_add_u32 m0, s20, 0xe000
	v_lshl_add_u64 v[20:21], v[10:11], 0, s[2:3]
	global_load_lds_dwordx4 v[20:21], off
	v_mfma_f32_16x16x32_f16 a[56:59], v[136:139], v[124:127], a[56:59]
	s_add_u32 m0, s20, 0xb000
	v_lshl_add_u64 v[20:21], v[0:1], 0, s[2:3]
	global_load_lds_dwordx4 v[20:21], off
	v_mfma_f32_16x16x32_f16 a[60:63], v[140:143], v[124:127], a[60:63]
	s_add_u32 m0, s20, 0xf000
	v_lshl_add_u64 v[20:21], v[8:9], 0, s[2:3]
	global_load_lds_dwordx4 v[20:21], off
	s_waitcnt lgkmcnt(0)
	v_mfma_f32_16x16x32_f16 a[0:3], v[96:99], v[80:83], a[0:3]
	ds_read_b128 v[112:115], v24 offset:32768
	v_mfma_f32_16x16x32_f16 a[4:7], v[100:103], v[80:83], a[4:7]
	ds_read_b128 v[128:131], v25 offset:49152
	v_mfma_f32_16x16x32_f16 a[8:11], v[104:107], v[80:83], a[8:11]
	ds_read_b128 v[116:119], v24 offset:34816
	v_mfma_f32_16x16x32_f16 a[12:15], v[108:111], v[80:83], a[12:15]
	ds_read_b128 v[132:135], v25 offset:51200
	v_mfma_f32_16x16x32_f16 a[16:19], v[96:99], v[84:87], a[16:19]
	ds_read_b128 v[120:123], v24 offset:36864
	v_mfma_f32_16x16x32_f16 a[20:23], v[100:103], v[84:87], a[20:23]
	ds_read_b128 v[136:139], v25 offset:53248
	v_mfma_f32_16x16x32_f16 a[24:27], v[104:107], v[84:87], a[24:27]
	ds_read_b128 v[124:127], v24 offset:38912
	v_mfma_f32_16x16x32_f16 a[28:31], v[108:111], v[84:87], a[28:31]
	ds_read_b128 v[140:143], v25 offset:55296
	v_mfma_f32_16x16x32_f16 a[32:35], v[96:99], v[88:91], a[32:35]
	v_mfma_f32_16x16x32_f16 a[36:39], v[100:103], v[88:91], a[36:39]
	v_mfma_f32_16x16x32_f16 a[40:43], v[104:107], v[88:91], a[40:43]
	v_mfma_f32_16x16x32_f16 a[44:47], v[108:111], v[88:91], a[44:47]
	v_mfma_f32_16x16x32_f16 a[48:51], v[96:99], v[92:95], a[48:51]
	v_mfma_f32_16x16x32_f16 a[52:55], v[100:103], v[92:95], a[52:55]
	v_mfma_f32_16x16x32_f16 a[56:59], v[104:107], v[92:95], a[56:59]
	v_mfma_f32_16x16x32_f16 a[60:63], v[108:111], v[92:95], a[60:63]
	s_waitcnt vmcnt(8)
	s_barrier
	s_mov_b64 s[2:3], 0x280
	s_waitcnt lgkmcnt(0)
	v_mfma_f32_16x16x32_f16 a[0:3], v[128:131], v[112:115], a[0:3]
	ds_read_b128 v[80:83], v17
	v_mfma_f32_16x16x32_f16 a[4:7], v[132:135], v[112:115], a[4:7]
	ds_read_b128 v[96:99], v16 offset:16384
	v_mfma_f32_16x16x32_f16 a[8:11], v[136:139], v[112:115], a[8:11]
	ds_read_b128 v[84:87], v17 offset:2048
	v_mfma_f32_16x16x32_f16 a[12:15], v[140:143], v[112:115], a[12:15]
	ds_read_b128 v[100:103], v16 offset:18432
	v_mfma_f32_16x16x32_f16 a[16:19], v[128:131], v[116:119], a[16:19]
	ds_read_b128 v[88:91], v17 offset:4096
	v_mfma_f32_16x16x32_f16 a[20:23], v[132:135], v[116:119], a[20:23]
	ds_read_b128 v[104:107], v16 offset:20480
	v_mfma_f32_16x16x32_f16 a[24:27], v[136:139], v[116:119], a[24:27]
	ds_read_b128 v[92:95], v17 offset:6144
	v_mfma_f32_16x16x32_f16 a[28:31], v[140:143], v[116:119], a[28:31]
	ds_read_b128 v[108:111], v16 offset:22528
	v_mfma_f32_16x16x32_f16 a[32:35], v[128:131], v[120:123], a[32:35]
	s_add_u32 m0, s20, 0x10000
	v_lshl_add_u64 v[20:21], v[6:7], 0, s[2:3]
	global_load_lds_dwordx4 v[20:21], off
	v_mfma_f32_16x16x32_f16 a[36:39], v[132:135], v[120:123], a[36:39]
	s_add_u32 m0, s20, 0x14000
	v_lshl_add_u64 v[20:21], v[14:15], 0, s[2:3]
	global_load_lds_dwordx4 v[20:21], off
	v_mfma_f32_16x16x32_f16 a[40:43], v[136:139], v[120:123], a[40:43]
	s_add_u32 m0, s20, 0x11000
	v_lshl_add_u64 v[20:21], v[4:5], 0, s[2:3]
	global_load_lds_dwordx4 v[20:21], off
	v_mfma_f32_16x16x32_f16 a[44:47], v[140:143], v[120:123], a[44:47]
	s_add_u32 m0, s20, 0x15000
	v_lshl_add_u64 v[20:21], v[12:13], 0, s[2:3]
	global_load_lds_dwordx4 v[20:21], off
	v_mfma_f32_16x16x32_f16 a[48:51], v[128:131], v[124:127], a[48:51]
	s_add_u32 m0, s20, 0x12000
	v_lshl_add_u64 v[20:21], v[2:3], 0, s[2:3]
	global_load_lds_dwordx4 v[20:21], off
	v_mfma_f32_16x16x32_f16 a[52:55], v[132:135], v[124:127], a[52:55]
	s_add_u32 m0, s20, 0x16000
	v_lshl_add_u64 v[20:21], v[10:11], 0, s[2:3]
	global_load_lds_dwordx4 v[20:21], off
	v_mfma_f32_16x16x32_f16 a[56:59], v[136:139], v[124:127], a[56:59]
	s_add_u32 m0, s20, 0x13000
	v_lshl_add_u64 v[20:21], v[0:1], 0, s[2:3]
	global_load_lds_dwordx4 v[20:21], off
	v_mfma_f32_16x16x32_f16 a[60:63], v[140:143], v[124:127], a[60:63]
	s_add_u32 m0, s20, 0x17000
	v_lshl_add_u64 v[20:21], v[8:9], 0, s[2:3]
	global_load_lds_dwordx4 v[20:21], off
	s_waitcnt lgkmcnt(0)
	v_mfma_f32_16x16x32_f16 a[0:3], v[96:99], v[80:83], a[0:3]
	ds_read_b128 v[112:115], v18
	v_mfma_f32_16x16x32_f16 a[4:7], v[100:103], v[80:83], a[4:7]
	ds_read_b128 v[128:131], v19 offset:16384
	v_mfma_f32_16x16x32_f16 a[8:11], v[104:107], v[80:83], a[8:11]
	ds_read_b128 v[116:119], v18 offset:2048
	v_mfma_f32_16x16x32_f16 a[12:15], v[108:111], v[80:83], a[12:15]
	ds_read_b128 v[132:135], v19 offset:18432
	v_mfma_f32_16x16x32_f16 a[16:19], v[96:99], v[84:87], a[16:19]
	ds_read_b128 v[120:123], v18 offset:4096
	v_mfma_f32_16x16x32_f16 a[20:23], v[100:103], v[84:87], a[20:23]
	ds_read_b128 v[136:139], v19 offset:20480
	v_mfma_f32_16x16x32_f16 a[24:27], v[104:107], v[84:87], a[24:27]
	ds_read_b128 v[124:127], v18 offset:6144
	v_mfma_f32_16x16x32_f16 a[28:31], v[108:111], v[84:87], a[28:31]
	ds_read_b128 v[140:143], v19 offset:22528
	v_mfma_f32_16x16x32_f16 a[32:35], v[96:99], v[88:91], a[32:35]
	v_mfma_f32_16x16x32_f16 a[36:39], v[100:103], v[88:91], a[36:39]
	v_mfma_f32_16x16x32_f16 a[40:43], v[104:107], v[88:91], a[40:43]
	v_mfma_f32_16x16x32_f16 a[44:47], v[108:111], v[88:91], a[44:47]
	v_mfma_f32_16x16x32_f16 a[48:51], v[96:99], v[92:95], a[48:51]
	v_mfma_f32_16x16x32_f16 a[52:55], v[100:103], v[92:95], a[52:55]
	v_mfma_f32_16x16x32_f16 a[56:59], v[104:107], v[92:95], a[56:59]
	v_mfma_f32_16x16x32_f16 a[60:63], v[108:111], v[92:95], a[60:63]
	s_waitcnt vmcnt(8)
	s_barrier
	s_mov_b64 s[2:3], 0x300
	s_waitcnt lgkmcnt(0)
	v_mfma_f32_16x16x32_f16 a[0:3], v[128:131], v[112:115], a[0:3]
	ds_read_b128 v[80:83], v17 offset:32768
	v_mfma_f32_16x16x32_f16 a[4:7], v[132:135], v[112:115], a[4:7]
	ds_read_b128 v[96:99], v16 offset:49152
	v_mfma_f32_16x16x32_f16 a[8:11], v[136:139], v[112:115], a[8:11]
	ds_read_b128 v[84:87], v17 offset:34816
	v_mfma_f32_16x16x32_f16 a[12:15], v[140:143], v[112:115], a[12:15]
	ds_read_b128 v[100:103], v16 offset:51200
	v_mfma_f32_16x16x32_f16 a[16:19], v[128:131], v[116:119], a[16:19]
	ds_read_b128 v[88:91], v17 offset:36864
	v_mfma_f32_16x16x32_f16 a[20:23], v[132:135], v[116:119], a[20:23]
	ds_read_b128 v[104:107], v16 offset:53248
	v_mfma_f32_16x16x32_f16 a[24:27], v[136:139], v[116:119], a[24:27]
	ds_read_b128 v[92:95], v17 offset:38912
	v_mfma_f32_16x16x32_f16 a[28:31], v[140:143], v[116:119], a[28:31]
	ds_read_b128 v[108:111], v16 offset:55296
	v_mfma_f32_16x16x32_f16 a[32:35], v[128:131], v[120:123], a[32:35]
	s_add_u32 m0, s20, 0x18000
	v_lshl_add_u64 v[20:21], v[6:7], 0, s[2:3]
	global_load_lds_dwordx4 v[20:21], off
	v_mfma_f32_16x16x32_f16 a[36:39], v[132:135], v[120:123], a[36:39]
	s_add_u32 m0, s20, 0x1c000
	v_lshl_add_u64 v[20:21], v[14:15], 0, s[2:3]
	global_load_lds_dwordx4 v[20:21], off
	v_mfma_f32_16x16x32_f16 a[40:43], v[136:139], v[120:123], a[40:43]
	s_add_u32 m0, s20, 0x19000
	v_lshl_add_u64 v[20:21], v[4:5], 0, s[2:3]
	global_load_lds_dwordx4 v[20:21], off
	v_mfma_f32_16x16x32_f16 a[44:47], v[140:143], v[120:123], a[44:47]
	s_add_u32 m0, s20, 0x1d000
	v_lshl_add_u64 v[20:21], v[12:13], 0, s[2:3]
	global_load_lds_dwordx4 v[20:21], off
	v_mfma_f32_16x16x32_f16 a[48:51], v[128:131], v[124:127], a[48:51]
	s_add_u32 m0, s20, 0x1a000
	v_lshl_add_u64 v[20:21], v[2:3], 0, s[2:3]
	global_load_lds_dwordx4 v[20:21], off
	v_mfma_f32_16x16x32_f16 a[52:55], v[132:135], v[124:127], a[52:55]
	s_add_u32 m0, s20, 0x1e000
	v_lshl_add_u64 v[20:21], v[10:11], 0, s[2:3]
	global_load_lds_dwordx4 v[20:21], off
	v_mfma_f32_16x16x32_f16 a[56:59], v[136:139], v[124:127], a[56:59]
	s_add_u32 m0, s20, 0x1b000
	v_lshl_add_u64 v[20:21], v[0:1], 0, s[2:3]
	global_load_lds_dwordx4 v[20:21], off
	v_mfma_f32_16x16x32_f16 a[60:63], v[140:143], v[124:127], a[60:63]
	s_add_u32 m0, s20, 0x1f000
	v_lshl_add_u64 v[20:21], v[8:9], 0, s[2:3]
	global_load_lds_dwordx4 v[20:21], off
	s_waitcnt lgkmcnt(0)
	v_mfma_f32_16x16x32_f16 a[0:3], v[96:99], v[80:83], a[0:3]
	ds_read_b128 v[112:115], v18 offset:32768
	v_mfma_f32_16x16x32_f16 a[4:7], v[100:103], v[80:83], a[4:7]
	ds_read_b128 v[128:131], v19 offset:49152
	v_mfma_f32_16x16x32_f16 a[8:11], v[104:107], v[80:83], a[8:11]
	ds_read_b128 v[116:119], v18 offset:34816
	v_mfma_f32_16x16x32_f16 a[12:15], v[108:111], v[80:83], a[12:15]
	ds_read_b128 v[132:135], v19 offset:51200
	v_mfma_f32_16x16x32_f16 a[16:19], v[96:99], v[84:87], a[16:19]
	ds_read_b128 v[120:123], v18 offset:36864
	v_mfma_f32_16x16x32_f16 a[20:23], v[100:103], v[84:87], a[20:23]
	ds_read_b128 v[136:139], v19 offset:53248
	v_mfma_f32_16x16x32_f16 a[24:27], v[104:107], v[84:87], a[24:27]
	ds_read_b128 v[124:127], v18 offset:38912
	v_mfma_f32_16x16x32_f16 a[28:31], v[108:111], v[84:87], a[28:31]
	ds_read_b128 v[140:143], v19 offset:55296
	v_mfma_f32_16x16x32_f16 a[32:35], v[96:99], v[88:91], a[32:35]
	v_mfma_f32_16x16x32_f16 a[36:39], v[100:103], v[88:91], a[36:39]
	v_mfma_f32_16x16x32_f16 a[40:43], v[104:107], v[88:91], a[40:43]
	v_mfma_f32_16x16x32_f16 a[44:47], v[108:111], v[88:91], a[44:47]
	v_mfma_f32_16x16x32_f16 a[48:51], v[96:99], v[92:95], a[48:51]
	v_mfma_f32_16x16x32_f16 a[52:55], v[100:103], v[92:95], a[52:55]
	v_mfma_f32_16x16x32_f16 a[56:59], v[104:107], v[92:95], a[56:59]
	v_mfma_f32_16x16x32_f16 a[60:63], v[108:111], v[92:95], a[60:63]
	s_waitcnt vmcnt(8)
	s_barrier
	s_mov_b64 s[2:3], 0x380
	s_waitcnt lgkmcnt(0)
	v_mfma_f32_16x16x32_f16 a[0:3], v[128:131], v[112:115], a[0:3]
	ds_read_b128 v[80:83], v23
	v_mfma_f32_16x16x32_f16 a[4:7], v[132:135], v[112:115], a[4:7]
	ds_read_b128 v[96:99], v22 offset:16384
	v_mfma_f32_16x16x32_f16 a[8:11], v[136:139], v[112:115], a[8:11]
	ds_read_b128 v[84:87], v23 offset:2048
	v_mfma_f32_16x16x32_f16 a[12:15], v[140:143], v[112:115], a[12:15]
	ds_read_b128 v[100:103], v22 offset:18432
	v_mfma_f32_16x16x32_f16 a[16:19], v[128:131], v[116:119], a[16:19]
	ds_read_b128 v[88:91], v23 offset:4096
	v_mfma_f32_16x16x32_f16 a[20:23], v[132:135], v[116:119], a[20:23]
	ds_read_b128 v[104:107], v22 offset:20480
	v_mfma_f32_16x16x32_f16 a[24:27], v[136:139], v[116:119], a[24:27]
	ds_read_b128 v[92:95], v23 offset:6144
	v_mfma_f32_16x16x32_f16 a[28:31], v[140:143], v[116:119], a[28:31]
	ds_read_b128 v[108:111], v22 offset:22528
	v_mfma_f32_16x16x32_f16 a[32:35], v[128:131], v[120:123], a[32:35]
	s_add_u32 m0, s20, 0x0
	v_lshl_add_u64 v[20:21], v[6:7], 0, s[2:3]
	global_load_lds_dwordx4 v[20:21], off
	v_mfma_f32_16x16x32_f16 a[36:39], v[132:135], v[120:123], a[36:39]
	s_add_u32 m0, s20, 0x4000
	v_lshl_add_u64 v[20:21], v[14:15], 0, s[2:3]
	global_load_lds_dwordx4 v[20:21], off
	v_mfma_f32_16x16x32_f16 a[40:43], v[136:139], v[120:123], a[40:43]
	s_add_u32 m0, s20, 0x1000
	v_lshl_add_u64 v[20:21], v[4:5], 0, s[2:3]
	global_load_lds_dwordx4 v[20:21], off
	v_mfma_f32_16x16x32_f16 a[44:47], v[140:143], v[120:123], a[44:47]
	s_add_u32 m0, s20, 0x5000
	v_lshl_add_u64 v[20:21], v[12:13], 0, s[2:3]
	global_load_lds_dwordx4 v[20:21], off
	v_mfma_f32_16x16x32_f16 a[48:51], v[128:131], v[124:127], a[48:51]
	s_add_u32 m0, s20, 0x2000
	v_lshl_add_u64 v[20:21], v[2:3], 0, s[2:3]
	global_load_lds_dwordx4 v[20:21], off
	v_mfma_f32_16x16x32_f16 a[52:55], v[132:135], v[124:127], a[52:55]
	s_add_u32 m0, s20, 0x6000
	v_lshl_add_u64 v[20:21], v[10:11], 0, s[2:3]
	global_load_lds_dwordx4 v[20:21], off
	v_mfma_f32_16x16x32_f16 a[56:59], v[136:139], v[124:127], a[56:59]
	s_add_u32 m0, s20, 0x3000
	v_lshl_add_u64 v[20:21], v[0:1], 0, s[2:3]
	global_load_lds_dwordx4 v[20:21], off
	v_mfma_f32_16x16x32_f16 a[60:63], v[140:143], v[124:127], a[60:63]
	s_add_u32 m0, s20, 0x7000
	v_lshl_add_u64 v[20:21], v[8:9], 0, s[2:3]
	global_load_lds_dwordx4 v[20:21], off
	s_waitcnt lgkmcnt(0)
	v_mfma_f32_16x16x32_f16 a[0:3], v[96:99], v[80:83], a[0:3]
	ds_read_b128 v[112:115], v24
	v_mfma_f32_16x16x32_f16 a[4:7], v[100:103], v[80:83], a[4:7]
	ds_read_b128 v[128:131], v25 offset:16384
	v_mfma_f32_16x16x32_f16 a[8:11], v[104:107], v[80:83], a[8:11]
	ds_read_b128 v[116:119], v24 offset:2048
	v_mfma_f32_16x16x32_f16 a[12:15], v[108:111], v[80:83], a[12:15]
	ds_read_b128 v[132:135], v25 offset:18432
	v_mfma_f32_16x16x32_f16 a[16:19], v[96:99], v[84:87], a[16:19]
	ds_read_b128 v[120:123], v24 offset:4096
	v_mfma_f32_16x16x32_f16 a[20:23], v[100:103], v[84:87], a[20:23]
	ds_read_b128 v[136:139], v25 offset:20480
	v_mfma_f32_16x16x32_f16 a[24:27], v[104:107], v[84:87], a[24:27]
	ds_read_b128 v[124:127], v24 offset:6144
	v_mfma_f32_16x16x32_f16 a[28:31], v[108:111], v[84:87], a[28:31]
	ds_read_b128 v[140:143], v25 offset:22528
	v_mfma_f32_16x16x32_f16 a[32:35], v[96:99], v[88:91], a[32:35]
	v_mfma_f32_16x16x32_f16 a[36:39], v[100:103], v[88:91], a[36:39]
	v_mfma_f32_16x16x32_f16 a[40:43], v[104:107], v[88:91], a[40:43]
	v_mfma_f32_16x16x32_f16 a[44:47], v[108:111], v[88:91], a[44:47]
	v_mfma_f32_16x16x32_f16 a[48:51], v[96:99], v[92:95], a[48:51]
	v_mfma_f32_16x16x32_f16 a[52:55], v[100:103], v[92:95], a[52:55]
	v_mfma_f32_16x16x32_f16 a[56:59], v[104:107], v[92:95], a[56:59]
	v_mfma_f32_16x16x32_f16 a[60:63], v[108:111], v[92:95], a[60:63]
	s_waitcnt vmcnt(8)
	s_barrier
	s_mov_b64 s[2:3], 0x400
	s_waitcnt lgkmcnt(0)
	v_mfma_f32_16x16x32_f16 a[0:3], v[128:131], v[112:115], a[0:3]
	ds_read_b128 v[80:83], v23 offset:32768
	v_mfma_f32_16x16x32_f16 a[4:7], v[132:135], v[112:115], a[4:7]
	ds_read_b128 v[96:99], v22 offset:49152
	v_mfma_f32_16x16x32_f16 a[8:11], v[136:139], v[112:115], a[8:11]
	ds_read_b128 v[84:87], v23 offset:34816
	v_mfma_f32_16x16x32_f16 a[12:15], v[140:143], v[112:115], a[12:15]
	ds_read_b128 v[100:103], v22 offset:51200
	v_mfma_f32_16x16x32_f16 a[16:19], v[128:131], v[116:119], a[16:19]
	ds_read_b128 v[88:91], v23 offset:36864
	v_mfma_f32_16x16x32_f16 a[20:23], v[132:135], v[116:119], a[20:23]
	ds_read_b128 v[104:107], v22 offset:53248
	v_mfma_f32_16x16x32_f16 a[24:27], v[136:139], v[116:119], a[24:27]
	ds_read_b128 v[92:95], v23 offset:38912
	v_mfma_f32_16x16x32_f16 a[28:31], v[140:143], v[116:119], a[28:31]
	ds_read_b128 v[108:111], v22 offset:55296
	v_mfma_f32_16x16x32_f16 a[32:35], v[128:131], v[120:123], a[32:35]
	s_add_u32 m0, s20, 0x8000
	v_lshl_add_u64 v[20:21], v[6:7], 0, s[2:3]
	global_load_lds_dwordx4 v[20:21], off
	v_mfma_f32_16x16x32_f16 a[36:39], v[132:135], v[120:123], a[36:39]
	s_add_u32 m0, s20, 0xc000
	v_lshl_add_u64 v[20:21], v[14:15], 0, s[2:3]
	global_load_lds_dwordx4 v[20:21], off
	v_mfma_f32_16x16x32_f16 a[40:43], v[136:139], v[120:123], a[40:43]
	s_add_u32 m0, s20, 0x9000
	v_lshl_add_u64 v[20:21], v[4:5], 0, s[2:3]
	global_load_lds_dwordx4 v[20:21], off
	v_mfma_f32_16x16x32_f16 a[44:47], v[140:143], v[120:123], a[44:47]
	s_add_u32 m0, s20, 0xd000
	v_lshl_add_u64 v[20:21], v[12:13], 0, s[2:3]
	global_load_lds_dwordx4 v[20:21], off
	v_mfma_f32_16x16x32_f16 a[48:51], v[128:131], v[124:127], a[48:51]
	s_add_u32 m0, s20, 0xa000
	v_lshl_add_u64 v[20:21], v[2:3], 0, s[2:3]
	global_load_lds_dwordx4 v[20:21], off
	v_mfma_f32_16x16x32_f16 a[52:55], v[132:135], v[124:127], a[52:55]
	s_add_u32 m0, s20, 0xe000
	v_lshl_add_u64 v[20:21], v[10:11], 0, s[2:3]
	global_load_lds_dwordx4 v[20:21], off
	v_mfma_f32_16x16x32_f16 a[56:59], v[136:139], v[124:127], a[56:59]
	s_add_u32 m0, s20, 0xb000
	v_lshl_add_u64 v[20:21], v[0:1], 0, s[2:3]
	global_load_lds_dwordx4 v[20:21], off
	v_mfma_f32_16x16x32_f16 a[60:63], v[140:143], v[124:127], a[60:63]
	s_add_u32 m0, s20, 0xf000
	v_lshl_add_u64 v[20:21], v[8:9], 0, s[2:3]
	global_load_lds_dwordx4 v[20:21], off
	s_waitcnt lgkmcnt(0)
	v_mfma_f32_16x16x32_f16 a[0:3], v[96:99], v[80:83], a[0:3]
	ds_read_b128 v[112:115], v24 offset:32768
	v_mfma_f32_16x16x32_f16 a[4:7], v[100:103], v[80:83], a[4:7]
	ds_read_b128 v[128:131], v25 offset:49152
	v_mfma_f32_16x16x32_f16 a[8:11], v[104:107], v[80:83], a[8:11]
	ds_read_b128 v[116:119], v24 offset:34816
	v_mfma_f32_16x16x32_f16 a[12:15], v[108:111], v[80:83], a[12:15]
	ds_read_b128 v[132:135], v25 offset:51200
	v_mfma_f32_16x16x32_f16 a[16:19], v[96:99], v[84:87], a[16:19]
	ds_read_b128 v[120:123], v24 offset:36864
	v_mfma_f32_16x16x32_f16 a[20:23], v[100:103], v[84:87], a[20:23]
	ds_read_b128 v[136:139], v25 offset:53248
	v_mfma_f32_16x16x32_f16 a[24:27], v[104:107], v[84:87], a[24:27]
	ds_read_b128 v[124:127], v24 offset:38912
	v_mfma_f32_16x16x32_f16 a[28:31], v[108:111], v[84:87], a[28:31]
	ds_read_b128 v[140:143], v25 offset:55296
	v_mfma_f32_16x16x32_f16 a[32:35], v[96:99], v[88:91], a[32:35]
	v_mfma_f32_16x16x32_f16 a[36:39], v[100:103], v[88:91], a[36:39]
	v_mfma_f32_16x16x32_f16 a[40:43], v[104:107], v[88:91], a[40:43]
	v_mfma_f32_16x16x32_f16 a[44:47], v[108:111], v[88:91], a[44:47]
	v_mfma_f32_16x16x32_f16 a[48:51], v[96:99], v[92:95], a[48:51]
	v_mfma_f32_16x16x32_f16 a[52:55], v[100:103], v[92:95], a[52:55]
	v_mfma_f32_16x16x32_f16 a[56:59], v[104:107], v[92:95], a[56:59]
	v_mfma_f32_16x16x32_f16 a[60:63], v[108:111], v[92:95], a[60:63]
	s_waitcnt vmcnt(8)
	s_barrier
	s_mov_b64 s[2:3], 0x480
	s_waitcnt lgkmcnt(0)
	v_mfma_f32_16x16x32_f16 a[0:3], v[128:131], v[112:115], a[0:3]
	ds_read_b128 v[80:83], v17
	v_mfma_f32_16x16x32_f16 a[4:7], v[132:135], v[112:115], a[4:7]
	ds_read_b128 v[96:99], v16 offset:16384
	v_mfma_f32_16x16x32_f16 a[8:11], v[136:139], v[112:115], a[8:11]
	ds_read_b128 v[84:87], v17 offset:2048
	v_mfma_f32_16x16x32_f16 a[12:15], v[140:143], v[112:115], a[12:15]
	ds_read_b128 v[100:103], v16 offset:18432
	v_mfma_f32_16x16x32_f16 a[16:19], v[128:131], v[116:119], a[16:19]
	ds_read_b128 v[88:91], v17 offset:4096
	v_mfma_f32_16x16x32_f16 a[20:23], v[132:135], v[116:119], a[20:23]
	ds_read_b128 v[104:107], v16 offset:20480
	v_mfma_f32_16x16x32_f16 a[24:27], v[136:139], v[116:119], a[24:27]
	ds_read_b128 v[92:95], v17 offset:6144
	v_mfma_f32_16x16x32_f16 a[28:31], v[140:143], v[116:119], a[28:31]
	ds_read_b128 v[108:111], v16 offset:22528
	v_mfma_f32_16x16x32_f16 a[32:35], v[128:131], v[120:123], a[32:35]
	s_add_u32 m0, s20, 0x10000
	v_lshl_add_u64 v[20:21], v[6:7], 0, s[2:3]
	global_load_lds_dwordx4 v[20:21], off
	v_mfma_f32_16x16x32_f16 a[36:39], v[132:135], v[120:123], a[36:39]
	s_add_u32 m0, s20, 0x14000
	v_lshl_add_u64 v[20:21], v[14:15], 0, s[2:3]
	global_load_lds_dwordx4 v[20:21], off
	v_mfma_f32_16x16x32_f16 a[40:43], v[136:139], v[120:123], a[40:43]
	s_add_u32 m0, s20, 0x11000
	v_lshl_add_u64 v[20:21], v[4:5], 0, s[2:3]
	global_load_lds_dwordx4 v[20:21], off
	v_mfma_f32_16x16x32_f16 a[44:47], v[140:143], v[120:123], a[44:47]
	s_add_u32 m0, s20, 0x15000
	v_lshl_add_u64 v[20:21], v[12:13], 0, s[2:3]
	global_load_lds_dwordx4 v[20:21], off
	v_mfma_f32_16x16x32_f16 a[48:51], v[128:131], v[124:127], a[48:51]
	s_add_u32 m0, s20, 0x12000
	v_lshl_add_u64 v[20:21], v[2:3], 0, s[2:3]
	global_load_lds_dwordx4 v[20:21], off
	v_mfma_f32_16x16x32_f16 a[52:55], v[132:135], v[124:127], a[52:55]
	s_add_u32 m0, s20, 0x16000
	v_lshl_add_u64 v[20:21], v[10:11], 0, s[2:3]
	global_load_lds_dwordx4 v[20:21], off
	v_mfma_f32_16x16x32_f16 a[56:59], v[136:139], v[124:127], a[56:59]
	s_add_u32 m0, s20, 0x13000
	v_lshl_add_u64 v[20:21], v[0:1], 0, s[2:3]
	global_load_lds_dwordx4 v[20:21], off
	v_mfma_f32_16x16x32_f16 a[60:63], v[140:143], v[124:127], a[60:63]
	s_add_u32 m0, s20, 0x17000
	v_lshl_add_u64 v[20:21], v[8:9], 0, s[2:3]
	global_load_lds_dwordx4 v[20:21], off
	s_waitcnt lgkmcnt(0)
	v_mfma_f32_16x16x32_f16 a[0:3], v[96:99], v[80:83], a[0:3]
	ds_read_b128 v[112:115], v18
	v_mfma_f32_16x16x32_f16 a[4:7], v[100:103], v[80:83], a[4:7]
	ds_read_b128 v[128:131], v19 offset:16384
	v_mfma_f32_16x16x32_f16 a[8:11], v[104:107], v[80:83], a[8:11]
	ds_read_b128 v[116:119], v18 offset:2048
	v_mfma_f32_16x16x32_f16 a[12:15], v[108:111], v[80:83], a[12:15]
	ds_read_b128 v[132:135], v19 offset:18432
	v_mfma_f32_16x16x32_f16 a[16:19], v[96:99], v[84:87], a[16:19]
	ds_read_b128 v[120:123], v18 offset:4096
	v_mfma_f32_16x16x32_f16 a[20:23], v[100:103], v[84:87], a[20:23]
	ds_read_b128 v[136:139], v19 offset:20480
	v_mfma_f32_16x16x32_f16 a[24:27], v[104:107], v[84:87], a[24:27]
	ds_read_b128 v[124:127], v18 offset:6144
	v_mfma_f32_16x16x32_f16 a[28:31], v[108:111], v[84:87], a[28:31]
	ds_read_b128 v[140:143], v19 offset:22528
	v_mfma_f32_16x16x32_f16 a[32:35], v[96:99], v[88:91], a[32:35]
	v_mfma_f32_16x16x32_f16 a[36:39], v[100:103], v[88:91], a[36:39]
	v_mfma_f32_16x16x32_f16 a[40:43], v[104:107], v[88:91], a[40:43]
	v_mfma_f32_16x16x32_f16 a[44:47], v[108:111], v[88:91], a[44:47]
	v_mfma_f32_16x16x32_f16 a[48:51], v[96:99], v[92:95], a[48:51]
	v_mfma_f32_16x16x32_f16 a[52:55], v[100:103], v[92:95], a[52:55]
	v_mfma_f32_16x16x32_f16 a[56:59], v[104:107], v[92:95], a[56:59]
	v_mfma_f32_16x16x32_f16 a[60:63], v[108:111], v[92:95], a[60:63]
	s_waitcnt vmcnt(8)
	s_barrier
	s_mov_b64 s[2:3], 0x500
	s_waitcnt lgkmcnt(0)
	v_mfma_f32_16x16x32_f16 a[0:3], v[128:131], v[112:115], a[0:3]
	ds_read_b128 v[80:83], v17 offset:32768
	v_mfma_f32_16x16x32_f16 a[4:7], v[132:135], v[112:115], a[4:7]
	ds_read_b128 v[96:99], v16 offset:49152
	v_mfma_f32_16x16x32_f16 a[8:11], v[136:139], v[112:115], a[8:11]
	ds_read_b128 v[84:87], v17 offset:34816
	v_mfma_f32_16x16x32_f16 a[12:15], v[140:143], v[112:115], a[12:15]
	ds_read_b128 v[100:103], v16 offset:51200
	v_mfma_f32_16x16x32_f16 a[16:19], v[128:131], v[116:119], a[16:19]
	ds_read_b128 v[88:91], v17 offset:36864
	v_mfma_f32_16x16x32_f16 a[20:23], v[132:135], v[116:119], a[20:23]
	ds_read_b128 v[104:107], v16 offset:53248
	v_mfma_f32_16x16x32_f16 a[24:27], v[136:139], v[116:119], a[24:27]
	ds_read_b128 v[92:95], v17 offset:38912
	v_mfma_f32_16x16x32_f16 a[28:31], v[140:143], v[116:119], a[28:31]
	ds_read_b128 v[108:111], v16 offset:55296
	v_mfma_f32_16x16x32_f16 a[32:35], v[128:131], v[120:123], a[32:35]
	s_add_u32 m0, s20, 0x18000
	v_lshl_add_u64 v[20:21], v[6:7], 0, s[2:3]
	global_load_lds_dwordx4 v[20:21], off
	v_mfma_f32_16x16x32_f16 a[36:39], v[132:135], v[120:123], a[36:39]
	s_add_u32 m0, s20, 0x1c000
	v_lshl_add_u64 v[20:21], v[14:15], 0, s[2:3]
	global_load_lds_dwordx4 v[20:21], off
	v_mfma_f32_16x16x32_f16 a[40:43], v[136:139], v[120:123], a[40:43]
	s_add_u32 m0, s20, 0x19000
	v_lshl_add_u64 v[20:21], v[4:5], 0, s[2:3]
	global_load_lds_dwordx4 v[20:21], off
	v_mfma_f32_16x16x32_f16 a[44:47], v[140:143], v[120:123], a[44:47]
	s_add_u32 m0, s20, 0x1d000
	v_lshl_add_u64 v[20:21], v[12:13], 0, s[2:3]
	global_load_lds_dwordx4 v[20:21], off
	v_mfma_f32_16x16x32_f16 a[48:51], v[128:131], v[124:127], a[48:51]
	s_add_u32 m0, s20, 0x1a000
	v_lshl_add_u64 v[20:21], v[2:3], 0, s[2:3]
	global_load_lds_dwordx4 v[20:21], off
	v_mfma_f32_16x16x32_f16 a[52:55], v[132:135], v[124:127], a[52:55]
	s_add_u32 m0, s20, 0x1e000
	v_lshl_add_u64 v[20:21], v[10:11], 0, s[2:3]
	global_load_lds_dwordx4 v[20:21], off
	v_mfma_f32_16x16x32_f16 a[56:59], v[136:139], v[124:127], a[56:59]
	s_add_u32 m0, s20, 0x1b000
	v_lshl_add_u64 v[20:21], v[0:1], 0, s[2:3]
	global_load_lds_dwordx4 v[20:21], off
	v_mfma_f32_16x16x32_f16 a[60:63], v[140:143], v[124:127], a[60:63]
	s_add_u32 m0, s20, 0x1f000
	v_lshl_add_u64 v[20:21], v[8:9], 0, s[2:3]
	global_load_lds_dwordx4 v[20:21], off
	s_waitcnt lgkmcnt(0)
	v_mfma_f32_16x16x32_f16 a[0:3], v[96:99], v[80:83], a[0:3]
	ds_read_b128 v[112:115], v18 offset:32768
	v_mfma_f32_16x16x32_f16 a[4:7], v[100:103], v[80:83], a[4:7]
	ds_read_b128 v[128:131], v19 offset:49152
	v_mfma_f32_16x16x32_f16 a[8:11], v[104:107], v[80:83], a[8:11]
	ds_read_b128 v[116:119], v18 offset:34816
	v_mfma_f32_16x16x32_f16 a[12:15], v[108:111], v[80:83], a[12:15]
	ds_read_b128 v[132:135], v19 offset:51200
	v_mfma_f32_16x16x32_f16 a[16:19], v[96:99], v[84:87], a[16:19]
	ds_read_b128 v[120:123], v18 offset:36864
	v_mfma_f32_16x16x32_f16 a[20:23], v[100:103], v[84:87], a[20:23]
	ds_read_b128 v[136:139], v19 offset:53248
	v_mfma_f32_16x16x32_f16 a[24:27], v[104:107], v[84:87], a[24:27]
	ds_read_b128 v[124:127], v18 offset:38912
	v_mfma_f32_16x16x32_f16 a[28:31], v[108:111], v[84:87], a[28:31]
	ds_read_b128 v[140:143], v19 offset:55296
	v_mfma_f32_16x16x32_f16 a[32:35], v[96:99], v[88:91], a[32:35]
	v_mfma_f32_16x16x32_f16 a[36:39], v[100:103], v[88:91], a[36:39]
	v_mfma_f32_16x16x32_f16 a[40:43], v[104:107], v[88:91], a[40:43]
	v_mfma_f32_16x16x32_f16 a[44:47], v[108:111], v[88:91], a[44:47]
	v_mfma_f32_16x16x32_f16 a[48:51], v[96:99], v[92:95], a[48:51]
	v_mfma_f32_16x16x32_f16 a[52:55], v[100:103], v[92:95], a[52:55]
	v_mfma_f32_16x16x32_f16 a[56:59], v[104:107], v[92:95], a[56:59]
	v_mfma_f32_16x16x32_f16 a[60:63], v[108:111], v[92:95], a[60:63]
	s_waitcnt vmcnt(8)
	s_barrier
	s_mov_b64 s[2:3], 0x580
	s_waitcnt lgkmcnt(0)
	v_mfma_f32_16x16x32_f16 a[0:3], v[128:131], v[112:115], a[0:3]
	ds_read_b128 v[80:83], v23
	v_mfma_f32_16x16x32_f16 a[4:7], v[132:135], v[112:115], a[4:7]
	ds_read_b128 v[96:99], v22 offset:16384
	v_mfma_f32_16x16x32_f16 a[8:11], v[136:139], v[112:115], a[8:11]
	ds_read_b128 v[84:87], v23 offset:2048
	v_mfma_f32_16x16x32_f16 a[12:15], v[140:143], v[112:115], a[12:15]
	ds_read_b128 v[100:103], v22 offset:18432
	v_mfma_f32_16x16x32_f16 a[16:19], v[128:131], v[116:119], a[16:19]
	ds_read_b128 v[88:91], v23 offset:4096
	v_mfma_f32_16x16x32_f16 a[20:23], v[132:135], v[116:119], a[20:23]
	ds_read_b128 v[104:107], v22 offset:20480
	v_mfma_f32_16x16x32_f16 a[24:27], v[136:139], v[116:119], a[24:27]
	ds_read_b128 v[92:95], v23 offset:6144
	v_mfma_f32_16x16x32_f16 a[28:31], v[140:143], v[116:119], a[28:31]
	ds_read_b128 v[108:111], v22 offset:22528
	v_mfma_f32_16x16x32_f16 a[32:35], v[128:131], v[120:123], a[32:35]
	s_add_u32 m0, s20, 0x0
	v_lshl_add_u64 v[20:21], v[6:7], 0, s[2:3]
	global_load_lds_dwordx4 v[20:21], off
	v_mfma_f32_16x16x32_f16 a[36:39], v[132:135], v[120:123], a[36:39]
	s_add_u32 m0, s20, 0x4000
	v_lshl_add_u64 v[20:21], v[14:15], 0, s[2:3]
	global_load_lds_dwordx4 v[20:21], off
	v_mfma_f32_16x16x32_f16 a[40:43], v[136:139], v[120:123], a[40:43]
	s_add_u32 m0, s20, 0x1000
	v_lshl_add_u64 v[20:21], v[4:5], 0, s[2:3]
	global_load_lds_dwordx4 v[20:21], off
	v_mfma_f32_16x16x32_f16 a[44:47], v[140:143], v[120:123], a[44:47]
	s_add_u32 m0, s20, 0x5000
	v_lshl_add_u64 v[20:21], v[12:13], 0, s[2:3]
	global_load_lds_dwordx4 v[20:21], off
	v_mfma_f32_16x16x32_f16 a[48:51], v[128:131], v[124:127], a[48:51]
	s_add_u32 m0, s20, 0x2000
	v_lshl_add_u64 v[20:21], v[2:3], 0, s[2:3]
	global_load_lds_dwordx4 v[20:21], off
	v_mfma_f32_16x16x32_f16 a[52:55], v[132:135], v[124:127], a[52:55]
	s_add_u32 m0, s20, 0x6000
	v_lshl_add_u64 v[20:21], v[10:11], 0, s[2:3]
	global_load_lds_dwordx4 v[20:21], off
	v_mfma_f32_16x16x32_f16 a[56:59], v[136:139], v[124:127], a[56:59]
	s_add_u32 m0, s20, 0x3000
	v_lshl_add_u64 v[20:21], v[0:1], 0, s[2:3]
	global_load_lds_dwordx4 v[20:21], off
	v_mfma_f32_16x16x32_f16 a[60:63], v[140:143], v[124:127], a[60:63]
	s_add_u32 m0, s20, 0x7000
	v_lshl_add_u64 v[20:21], v[8:9], 0, s[2:3]
	global_load_lds_dwordx4 v[20:21], off
	s_waitcnt lgkmcnt(0)
	v_mfma_f32_16x16x32_f16 a[0:3], v[96:99], v[80:83], a[0:3]
	ds_read_b128 v[112:115], v24
	v_mfma_f32_16x16x32_f16 a[4:7], v[100:103], v[80:83], a[4:7]
	ds_read_b128 v[128:131], v25 offset:16384
	v_mfma_f32_16x16x32_f16 a[8:11], v[104:107], v[80:83], a[8:11]
	ds_read_b128 v[116:119], v24 offset:2048
	v_mfma_f32_16x16x32_f16 a[12:15], v[108:111], v[80:83], a[12:15]
	ds_read_b128 v[132:135], v25 offset:18432
	v_mfma_f32_16x16x32_f16 a[16:19], v[96:99], v[84:87], a[16:19]
	ds_read_b128 v[120:123], v24 offset:4096
	v_mfma_f32_16x16x32_f16 a[20:23], v[100:103], v[84:87], a[20:23]
	ds_read_b128 v[136:139], v25 offset:20480
	v_mfma_f32_16x16x32_f16 a[24:27], v[104:107], v[84:87], a[24:27]
	ds_read_b128 v[124:127], v24 offset:6144
	v_mfma_f32_16x16x32_f16 a[28:31], v[108:111], v[84:87], a[28:31]
	ds_read_b128 v[140:143], v25 offset:22528
	v_mfma_f32_16x16x32_f16 a[32:35], v[96:99], v[88:91], a[32:35]
	v_mfma_f32_16x16x32_f16 a[36:39], v[100:103], v[88:91], a[36:39]
	v_mfma_f32_16x16x32_f16 a[40:43], v[104:107], v[88:91], a[40:43]
	v_mfma_f32_16x16x32_f16 a[44:47], v[108:111], v[88:91], a[44:47]
	v_mfma_f32_16x16x32_f16 a[48:51], v[96:99], v[92:95], a[48:51]
	v_mfma_f32_16x16x32_f16 a[52:55], v[100:103], v[92:95], a[52:55]
	v_mfma_f32_16x16x32_f16 a[56:59], v[104:107], v[92:95], a[56:59]
	v_mfma_f32_16x16x32_f16 a[60:63], v[108:111], v[92:95], a[60:63]
	s_waitcnt vmcnt(8)
	s_barrier
	s_mov_b64 s[2:3], 0x600
	s_waitcnt lgkmcnt(0)
	v_mfma_f32_16x16x32_f16 a[0:3], v[128:131], v[112:115], a[0:3]
	ds_read_b128 v[80:83], v23 offset:32768
	v_mfma_f32_16x16x32_f16 a[4:7], v[132:135], v[112:115], a[4:7]
	ds_read_b128 v[96:99], v22 offset:49152
	v_mfma_f32_16x16x32_f16 a[8:11], v[136:139], v[112:115], a[8:11]
	ds_read_b128 v[84:87], v23 offset:34816
	v_mfma_f32_16x16x32_f16 a[12:15], v[140:143], v[112:115], a[12:15]
	ds_read_b128 v[100:103], v22 offset:51200
	v_mfma_f32_16x16x32_f16 a[16:19], v[128:131], v[116:119], a[16:19]
	ds_read_b128 v[88:91], v23 offset:36864
	v_mfma_f32_16x16x32_f16 a[20:23], v[132:135], v[116:119], a[20:23]
	ds_read_b128 v[104:107], v22 offset:53248
	v_mfma_f32_16x16x32_f16 a[24:27], v[136:139], v[116:119], a[24:27]
	ds_read_b128 v[92:95], v23 offset:38912
	v_mfma_f32_16x16x32_f16 a[28:31], v[140:143], v[116:119], a[28:31]
	ds_read_b128 v[108:111], v22 offset:55296
	v_mfma_f32_16x16x32_f16 a[32:35], v[128:131], v[120:123], a[32:35]
	s_add_u32 m0, s20, 0x8000
	v_lshl_add_u64 v[20:21], v[6:7], 0, s[2:3]
	global_load_lds_dwordx4 v[20:21], off
	v_mfma_f32_16x16x32_f16 a[36:39], v[132:135], v[120:123], a[36:39]
	s_add_u32 m0, s20, 0xc000
	v_lshl_add_u64 v[20:21], v[14:15], 0, s[2:3]
	global_load_lds_dwordx4 v[20:21], off
	v_mfma_f32_16x16x32_f16 a[40:43], v[136:139], v[120:123], a[40:43]
	s_add_u32 m0, s20, 0x9000
	v_lshl_add_u64 v[20:21], v[4:5], 0, s[2:3]
	global_load_lds_dwordx4 v[20:21], off
	v_mfma_f32_16x16x32_f16 a[44:47], v[140:143], v[120:123], a[44:47]
	s_add_u32 m0, s20, 0xd000
	v_lshl_add_u64 v[20:21], v[12:13], 0, s[2:3]
	global_load_lds_dwordx4 v[20:21], off
	v_mfma_f32_16x16x32_f16 a[48:51], v[128:131], v[124:127], a[48:51]
	s_add_u32 m0, s20, 0xa000
	v_lshl_add_u64 v[20:21], v[2:3], 0, s[2:3]
	global_load_lds_dwordx4 v[20:21], off
	v_mfma_f32_16x16x32_f16 a[52:55], v[132:135], v[124:127], a[52:55]
	s_add_u32 m0, s20, 0xe000
	v_lshl_add_u64 v[20:21], v[10:11], 0, s[2:3]
	global_load_lds_dwordx4 v[20:21], off
	v_mfma_f32_16x16x32_f16 a[56:59], v[136:139], v[124:127], a[56:59]
	s_add_u32 m0, s20, 0xb000
	v_lshl_add_u64 v[20:21], v[0:1], 0, s[2:3]
	global_load_lds_dwordx4 v[20:21], off
	v_mfma_f32_16x16x32_f16 a[60:63], v[140:143], v[124:127], a[60:63]
	s_add_u32 m0, s20, 0xf000
	v_lshl_add_u64 v[20:21], v[8:9], 0, s[2:3]
	global_load_lds_dwordx4 v[20:21], off
	s_waitcnt lgkmcnt(0)
	v_mfma_f32_16x16x32_f16 a[0:3], v[96:99], v[80:83], a[0:3]
	ds_read_b128 v[112:115], v24 offset:32768
	v_mfma_f32_16x16x32_f16 a[4:7], v[100:103], v[80:83], a[4:7]
	ds_read_b128 v[128:131], v25 offset:49152
	v_mfma_f32_16x16x32_f16 a[8:11], v[104:107], v[80:83], a[8:11]
	ds_read_b128 v[116:119], v24 offset:34816
	v_mfma_f32_16x16x32_f16 a[12:15], v[108:111], v[80:83], a[12:15]
	ds_read_b128 v[132:135], v25 offset:51200
	v_mfma_f32_16x16x32_f16 a[16:19], v[96:99], v[84:87], a[16:19]
	ds_read_b128 v[120:123], v24 offset:36864
	v_mfma_f32_16x16x32_f16 a[20:23], v[100:103], v[84:87], a[20:23]
	ds_read_b128 v[136:139], v25 offset:53248
	v_mfma_f32_16x16x32_f16 a[24:27], v[104:107], v[84:87], a[24:27]
	ds_read_b128 v[124:127], v24 offset:38912
	v_mfma_f32_16x16x32_f16 a[28:31], v[108:111], v[84:87], a[28:31]
	ds_read_b128 v[140:143], v25 offset:55296
	v_mfma_f32_16x16x32_f16 a[32:35], v[96:99], v[88:91], a[32:35]
	v_mfma_f32_16x16x32_f16 a[36:39], v[100:103], v[88:91], a[36:39]
	v_mfma_f32_16x16x32_f16 a[40:43], v[104:107], v[88:91], a[40:43]
	v_mfma_f32_16x16x32_f16 a[44:47], v[108:111], v[88:91], a[44:47]
	v_mfma_f32_16x16x32_f16 a[48:51], v[96:99], v[92:95], a[48:51]
	v_mfma_f32_16x16x32_f16 a[52:55], v[100:103], v[92:95], a[52:55]
	v_mfma_f32_16x16x32_f16 a[56:59], v[104:107], v[92:95], a[56:59]
	v_mfma_f32_16x16x32_f16 a[60:63], v[108:111], v[92:95], a[60:63]
	s_waitcnt vmcnt(8)
	s_barrier
	s_mov_b64 s[2:3], 0x680
	s_waitcnt lgkmcnt(0)
	v_mfma_f32_16x16x32_f16 a[0:3], v[128:131], v[112:115], a[0:3]
	ds_read_b128 v[80:83], v17
	v_mfma_f32_16x16x32_f16 a[4:7], v[132:135], v[112:115], a[4:7]
	ds_read_b128 v[96:99], v16 offset:16384
	v_mfma_f32_16x16x32_f16 a[8:11], v[136:139], v[112:115], a[8:11]
	ds_read_b128 v[84:87], v17 offset:2048
	v_mfma_f32_16x16x32_f16 a[12:15], v[140:143], v[112:115], a[12:15]
	ds_read_b128 v[100:103], v16 offset:18432
	v_mfma_f32_16x16x32_f16 a[16:19], v[128:131], v[116:119], a[16:19]
	ds_read_b128 v[88:91], v17 offset:4096
	v_mfma_f32_16x16x32_f16 a[20:23], v[132:135], v[116:119], a[20:23]
	ds_read_b128 v[104:107], v16 offset:20480
	v_mfma_f32_16x16x32_f16 a[24:27], v[136:139], v[116:119], a[24:27]
	ds_read_b128 v[92:95], v17 offset:6144
	v_mfma_f32_16x16x32_f16 a[28:31], v[140:143], v[116:119], a[28:31]
	ds_read_b128 v[108:111], v16 offset:22528
	v_mfma_f32_16x16x32_f16 a[32:35], v[128:131], v[120:123], a[32:35]
	s_add_u32 m0, s20, 0x10000
	v_lshl_add_u64 v[20:21], v[6:7], 0, s[2:3]
	global_load_lds_dwordx4 v[20:21], off
	v_mfma_f32_16x16x32_f16 a[36:39], v[132:135], v[120:123], a[36:39]
	s_add_u32 m0, s20, 0x14000
	v_lshl_add_u64 v[20:21], v[14:15], 0, s[2:3]
	global_load_lds_dwordx4 v[20:21], off
	v_mfma_f32_16x16x32_f16 a[40:43], v[136:139], v[120:123], a[40:43]
	s_add_u32 m0, s20, 0x11000
	v_lshl_add_u64 v[20:21], v[4:5], 0, s[2:3]
	global_load_lds_dwordx4 v[20:21], off
	v_mfma_f32_16x16x32_f16 a[44:47], v[140:143], v[120:123], a[44:47]
	s_add_u32 m0, s20, 0x15000
	v_lshl_add_u64 v[20:21], v[12:13], 0, s[2:3]
	global_load_lds_dwordx4 v[20:21], off
	v_mfma_f32_16x16x32_f16 a[48:51], v[128:131], v[124:127], a[48:51]
	s_add_u32 m0, s20, 0x12000
	v_lshl_add_u64 v[20:21], v[2:3], 0, s[2:3]
	global_load_lds_dwordx4 v[20:21], off
	v_mfma_f32_16x16x32_f16 a[52:55], v[132:135], v[124:127], a[52:55]
	s_add_u32 m0, s20, 0x16000
	v_lshl_add_u64 v[20:21], v[10:11], 0, s[2:3]
	global_load_lds_dwordx4 v[20:21], off
	v_mfma_f32_16x16x32_f16 a[56:59], v[136:139], v[124:127], a[56:59]
	s_add_u32 m0, s20, 0x13000
	v_lshl_add_u64 v[20:21], v[0:1], 0, s[2:3]
	global_load_lds_dwordx4 v[20:21], off
	v_mfma_f32_16x16x32_f16 a[60:63], v[140:143], v[124:127], a[60:63]
	s_add_u32 m0, s20, 0x17000
	v_lshl_add_u64 v[20:21], v[8:9], 0, s[2:3]
	global_load_lds_dwordx4 v[20:21], off
	s_waitcnt lgkmcnt(0)
	v_mfma_f32_16x16x32_f16 a[0:3], v[96:99], v[80:83], a[0:3]
	ds_read_b128 v[112:115], v18
	v_mfma_f32_16x16x32_f16 a[4:7], v[100:103], v[80:83], a[4:7]
	ds_read_b128 v[128:131], v19 offset:16384
	v_mfma_f32_16x16x32_f16 a[8:11], v[104:107], v[80:83], a[8:11]
	ds_read_b128 v[116:119], v18 offset:2048
	v_mfma_f32_16x16x32_f16 a[12:15], v[108:111], v[80:83], a[12:15]
	ds_read_b128 v[132:135], v19 offset:18432
	v_mfma_f32_16x16x32_f16 a[16:19], v[96:99], v[84:87], a[16:19]
	ds_read_b128 v[120:123], v18 offset:4096
	v_mfma_f32_16x16x32_f16 a[20:23], v[100:103], v[84:87], a[20:23]
	ds_read_b128 v[136:139], v19 offset:20480
	v_mfma_f32_16x16x32_f16 a[24:27], v[104:107], v[84:87], a[24:27]
	ds_read_b128 v[124:127], v18 offset:6144
	v_mfma_f32_16x16x32_f16 a[28:31], v[108:111], v[84:87], a[28:31]
	ds_read_b128 v[140:143], v19 offset:22528
	v_mfma_f32_16x16x32_f16 a[32:35], v[96:99], v[88:91], a[32:35]
	v_mfma_f32_16x16x32_f16 a[36:39], v[100:103], v[88:91], a[36:39]
	v_mfma_f32_16x16x32_f16 a[40:43], v[104:107], v[88:91], a[40:43]
	v_mfma_f32_16x16x32_f16 a[44:47], v[108:111], v[88:91], a[44:47]
	v_mfma_f32_16x16x32_f16 a[48:51], v[96:99], v[92:95], a[48:51]
	v_mfma_f32_16x16x32_f16 a[52:55], v[100:103], v[92:95], a[52:55]
	v_mfma_f32_16x16x32_f16 a[56:59], v[104:107], v[92:95], a[56:59]
	v_mfma_f32_16x16x32_f16 a[60:63], v[108:111], v[92:95], a[60:63]
	s_waitcnt vmcnt(8)
	s_barrier
	s_mov_b64 s[2:3], 0x700
	s_waitcnt lgkmcnt(0)
	v_mfma_f32_16x16x32_f16 a[0:3], v[128:131], v[112:115], a[0:3]
	ds_read_b128 v[80:83], v17 offset:32768
	v_mfma_f32_16x16x32_f16 a[4:7], v[132:135], v[112:115], a[4:7]
	ds_read_b128 v[96:99], v16 offset:49152
	v_mfma_f32_16x16x32_f16 a[8:11], v[136:139], v[112:115], a[8:11]
	ds_read_b128 v[84:87], v17 offset:34816
	v_mfma_f32_16x16x32_f16 a[12:15], v[140:143], v[112:115], a[12:15]
	ds_read_b128 v[100:103], v16 offset:51200
	v_mfma_f32_16x16x32_f16 a[16:19], v[128:131], v[116:119], a[16:19]
	ds_read_b128 v[88:91], v17 offset:36864
	v_mfma_f32_16x16x32_f16 a[20:23], v[132:135], v[116:119], a[20:23]
	ds_read_b128 v[104:107], v16 offset:53248
	v_mfma_f32_16x16x32_f16 a[24:27], v[136:139], v[116:119], a[24:27]
	ds_read_b128 v[92:95], v17 offset:38912
	v_mfma_f32_16x16x32_f16 a[28:31], v[140:143], v[116:119], a[28:31]
	ds_read_b128 v[108:111], v16 offset:55296
	v_mfma_f32_16x16x32_f16 a[32:35], v[128:131], v[120:123], a[32:35]
	s_add_u32 m0, s20, 0x18000
	v_lshl_add_u64 v[20:21], v[6:7], 0, s[2:3]
	global_load_lds_dwordx4 v[20:21], off
	v_mfma_f32_16x16x32_f16 a[36:39], v[132:135], v[120:123], a[36:39]
	s_add_u32 m0, s20, 0x1c000
	v_lshl_add_u64 v[20:21], v[14:15], 0, s[2:3]
	global_load_lds_dwordx4 v[20:21], off
	v_mfma_f32_16x16x32_f16 a[40:43], v[136:139], v[120:123], a[40:43]
	s_add_u32 m0, s20, 0x19000
	v_lshl_add_u64 v[20:21], v[4:5], 0, s[2:3]
	global_load_lds_dwordx4 v[20:21], off
	v_mfma_f32_16x16x32_f16 a[44:47], v[140:143], v[120:123], a[44:47]
	s_add_u32 m0, s20, 0x1d000
	v_lshl_add_u64 v[20:21], v[12:13], 0, s[2:3]
	global_load_lds_dwordx4 v[20:21], off
	v_mfma_f32_16x16x32_f16 a[48:51], v[128:131], v[124:127], a[48:51]
	s_add_u32 m0, s20, 0x1a000
	v_lshl_add_u64 v[20:21], v[2:3], 0, s[2:3]
	global_load_lds_dwordx4 v[20:21], off
	v_mfma_f32_16x16x32_f16 a[52:55], v[132:135], v[124:127], a[52:55]
	s_add_u32 m0, s20, 0x1e000
	v_lshl_add_u64 v[20:21], v[10:11], 0, s[2:3]
	global_load_lds_dwordx4 v[20:21], off
	v_mfma_f32_16x16x32_f16 a[56:59], v[136:139], v[124:127], a[56:59]
	s_add_u32 m0, s20, 0x1b000
	v_lshl_add_u64 v[20:21], v[0:1], 0, s[2:3]
	global_load_lds_dwordx4 v[20:21], off
	v_mfma_f32_16x16x32_f16 a[60:63], v[140:143], v[124:127], a[60:63]
	s_add_u32 m0, s20, 0x1f000
	v_lshl_add_u64 v[20:21], v[8:9], 0, s[2:3]
	global_load_lds_dwordx4 v[20:21], off
	s_waitcnt lgkmcnt(0)
	v_mfma_f32_16x16x32_f16 a[0:3], v[96:99], v[80:83], a[0:3]
	ds_read_b128 v[112:115], v18 offset:32768
	v_mfma_f32_16x16x32_f16 a[4:7], v[100:103], v[80:83], a[4:7]
	ds_read_b128 v[128:131], v19 offset:49152
	v_mfma_f32_16x16x32_f16 a[8:11], v[104:107], v[80:83], a[8:11]
	ds_read_b128 v[116:119], v18 offset:34816
	v_mfma_f32_16x16x32_f16 a[12:15], v[108:111], v[80:83], a[12:15]
	ds_read_b128 v[132:135], v19 offset:51200
	v_mfma_f32_16x16x32_f16 a[16:19], v[96:99], v[84:87], a[16:19]
	ds_read_b128 v[120:123], v18 offset:36864
	v_mfma_f32_16x16x32_f16 a[20:23], v[100:103], v[84:87], a[20:23]
	ds_read_b128 v[136:139], v19 offset:53248
	v_mfma_f32_16x16x32_f16 a[24:27], v[104:107], v[84:87], a[24:27]
	ds_read_b128 v[124:127], v18 offset:38912
	v_mfma_f32_16x16x32_f16 a[28:31], v[108:111], v[84:87], a[28:31]
	ds_read_b128 v[140:143], v19 offset:55296
	v_mfma_f32_16x16x32_f16 a[32:35], v[96:99], v[88:91], a[32:35]
	v_mfma_f32_16x16x32_f16 a[36:39], v[100:103], v[88:91], a[36:39]
	v_mfma_f32_16x16x32_f16 a[40:43], v[104:107], v[88:91], a[40:43]
	v_mfma_f32_16x16x32_f16 a[44:47], v[108:111], v[88:91], a[44:47]
	v_mfma_f32_16x16x32_f16 a[48:51], v[96:99], v[92:95], a[48:51]
	v_mfma_f32_16x16x32_f16 a[52:55], v[100:103], v[92:95], a[52:55]
	v_mfma_f32_16x16x32_f16 a[56:59], v[104:107], v[92:95], a[56:59]
	v_mfma_f32_16x16x32_f16 a[60:63], v[108:111], v[92:95], a[60:63]
	s_waitcnt vmcnt(8)
	s_barrier
	s_waitcnt lgkmcnt(0)
	v_mfma_f32_16x16x32_f16 a[0:3], v[128:131], v[112:115], a[0:3]
	ds_read_b128 v[80:83], v23
	v_mfma_f32_16x16x32_f16 a[4:7], v[132:135], v[112:115], a[4:7]
	ds_read_b128 v[96:99], v22 offset:16384
	v_mfma_f32_16x16x32_f16 a[8:11], v[136:139], v[112:115], a[8:11]
	ds_read_b128 v[84:87], v23 offset:2048
	v_mfma_f32_16x16x32_f16 a[12:15], v[140:143], v[112:115], a[12:15]
	ds_read_b128 v[100:103], v22 offset:18432
	v_mfma_f32_16x16x32_f16 a[16:19], v[128:131], v[116:119], a[16:19]
	ds_read_b128 v[88:91], v23 offset:4096
	v_mfma_f32_16x16x32_f16 a[20:23], v[132:135], v[116:119], a[20:23]
	ds_read_b128 v[104:107], v22 offset:20480
	v_mfma_f32_16x16x32_f16 a[24:27], v[136:139], v[116:119], a[24:27]
	ds_read_b128 v[92:95], v23 offset:6144
	v_mfma_f32_16x16x32_f16 a[28:31], v[140:143], v[116:119], a[28:31]
	ds_read_b128 v[108:111], v22 offset:22528
	v_mfma_f32_16x16x32_f16 a[32:35], v[128:131], v[120:123], a[32:35]
	v_mfma_f32_16x16x32_f16 a[36:39], v[132:135], v[120:123], a[36:39]
	v_mfma_f32_16x16x32_f16 a[40:43], v[136:139], v[120:123], a[40:43]
	v_mfma_f32_16x16x32_f16 a[44:47], v[140:143], v[120:123], a[44:47]
	v_mfma_f32_16x16x32_f16 a[48:51], v[128:131], v[124:127], a[48:51]
	v_mfma_f32_16x16x32_f16 a[52:55], v[132:135], v[124:127], a[52:55]
	v_mfma_f32_16x16x32_f16 a[56:59], v[136:139], v[124:127], a[56:59]
	v_mfma_f32_16x16x32_f16 a[60:63], v[140:143], v[124:127], a[60:63]
	s_waitcnt lgkmcnt(0)
	v_mfma_f32_16x16x32_f16 a[0:3], v[96:99], v[80:83], a[0:3]
	ds_read_b128 v[112:115], v24
	v_mfma_f32_16x16x32_f16 a[4:7], v[100:103], v[80:83], a[4:7]
	ds_read_b128 v[128:131], v25 offset:16384
	v_mfma_f32_16x16x32_f16 a[8:11], v[104:107], v[80:83], a[8:11]
	ds_read_b128 v[116:119], v24 offset:2048
	v_mfma_f32_16x16x32_f16 a[12:15], v[108:111], v[80:83], a[12:15]
	ds_read_b128 v[132:135], v25 offset:18432
	v_mfma_f32_16x16x32_f16 a[16:19], v[96:99], v[84:87], a[16:19]
	ds_read_b128 v[120:123], v24 offset:4096
	v_mfma_f32_16x16x32_f16 a[20:23], v[100:103], v[84:87], a[20:23]
	ds_read_b128 v[136:139], v25 offset:20480
	v_mfma_f32_16x16x32_f16 a[24:27], v[104:107], v[84:87], a[24:27]
	ds_read_b128 v[124:127], v24 offset:6144
	v_mfma_f32_16x16x32_f16 a[28:31], v[108:111], v[84:87], a[28:31]
	ds_read_b128 v[140:143], v25 offset:22528
	v_mfma_f32_16x16x32_f16 a[32:35], v[96:99], v[88:91], a[32:35]
	v_mfma_f32_16x16x32_f16 a[36:39], v[100:103], v[88:91], a[36:39]
	v_mfma_f32_16x16x32_f16 a[40:43], v[104:107], v[88:91], a[40:43]
	v_mfma_f32_16x16x32_f16 a[44:47], v[108:111], v[88:91], a[44:47]
	v_mfma_f32_16x16x32_f16 a[48:51], v[96:99], v[92:95], a[48:51]
	v_mfma_f32_16x16x32_f16 a[52:55], v[100:103], v[92:95], a[52:55]
	v_mfma_f32_16x16x32_f16 a[56:59], v[104:107], v[92:95], a[56:59]
	v_mfma_f32_16x16x32_f16 a[60:63], v[108:111], v[92:95], a[60:63]
	s_waitcnt vmcnt(0)
	s_barrier
	s_waitcnt lgkmcnt(0)
	v_mfma_f32_16x16x32_f16 a[0:3], v[128:131], v[112:115], a[0:3]
	ds_read_b128 v[80:83], v23 offset:32768
	v_mfma_f32_16x16x32_f16 a[4:7], v[132:135], v[112:115], a[4:7]
	ds_read_b128 v[96:99], v22 offset:49152
	v_mfma_f32_16x16x32_f16 a[8:11], v[136:139], v[112:115], a[8:11]
	ds_read_b128 v[84:87], v23 offset:34816
	v_mfma_f32_16x16x32_f16 a[12:15], v[140:143], v[112:115], a[12:15]
	ds_read_b128 v[100:103], v22 offset:51200
	v_mfma_f32_16x16x32_f16 a[16:19], v[128:131], v[116:119], a[16:19]
	ds_read_b128 v[88:91], v23 offset:36864
	v_mfma_f32_16x16x32_f16 a[20:23], v[132:135], v[116:119], a[20:23]
	ds_read_b128 v[104:107], v22 offset:53248
	v_mfma_f32_16x16x32_f16 a[24:27], v[136:139], v[116:119], a[24:27]
	ds_read_b128 v[92:95], v23 offset:38912
	v_mfma_f32_16x16x32_f16 a[28:31], v[140:143], v[116:119], a[28:31]
	ds_read_b128 v[108:111], v22 offset:55296
	v_mfma_f32_16x16x32_f16 a[32:35], v[128:131], v[120:123], a[32:35]
	v_mfma_f32_16x16x32_f16 a[36:39], v[132:135], v[120:123], a[36:39]
	v_mfma_f32_16x16x32_f16 a[40:43], v[136:139], v[120:123], a[40:43]
	v_mfma_f32_16x16x32_f16 a[44:47], v[140:143], v[120:123], a[44:47]
	v_mfma_f32_16x16x32_f16 a[48:51], v[128:131], v[124:127], a[48:51]
	v_mfma_f32_16x16x32_f16 a[52:55], v[132:135], v[124:127], a[52:55]
	v_mfma_f32_16x16x32_f16 a[56:59], v[136:139], v[124:127], a[56:59]
	v_mfma_f32_16x16x32_f16 a[60:63], v[140:143], v[124:127], a[60:63]
	s_waitcnt lgkmcnt(0)
	v_mfma_f32_16x16x32_f16 a[0:3], v[96:99], v[80:83], a[0:3]
	ds_read_b128 v[112:115], v24 offset:32768
	v_mfma_f32_16x16x32_f16 a[4:7], v[100:103], v[80:83], a[4:7]
	ds_read_b128 v[128:131], v25 offset:49152
	v_mfma_f32_16x16x32_f16 a[8:11], v[104:107], v[80:83], a[8:11]
	ds_read_b128 v[116:119], v24 offset:34816
	v_mfma_f32_16x16x32_f16 a[12:15], v[108:111], v[80:83], a[12:15]
	ds_read_b128 v[132:135], v25 offset:51200
	v_mfma_f32_16x16x32_f16 a[16:19], v[96:99], v[84:87], a[16:19]
	ds_read_b128 v[120:123], v24 offset:36864
	v_mfma_f32_16x16x32_f16 a[20:23], v[100:103], v[84:87], a[20:23]
	ds_read_b128 v[136:139], v25 offset:53248
	v_mfma_f32_16x16x32_f16 a[24:27], v[104:107], v[84:87], a[24:27]
	ds_read_b128 v[124:127], v24 offset:38912
	v_mfma_f32_16x16x32_f16 a[28:31], v[108:111], v[84:87], a[28:31]
	ds_read_b128 v[140:143], v25 offset:55296
	v_mfma_f32_16x16x32_f16 a[32:35], v[96:99], v[88:91], a[32:35]
	v_mfma_f32_16x16x32_f16 a[36:39], v[100:103], v[88:91], a[36:39]
	v_mfma_f32_16x16x32_f16 a[40:43], v[104:107], v[88:91], a[40:43]
	v_mfma_f32_16x16x32_f16 a[44:47], v[108:111], v[88:91], a[44:47]
	v_mfma_f32_16x16x32_f16 a[48:51], v[96:99], v[92:95], a[48:51]
	v_mfma_f32_16x16x32_f16 a[52:55], v[100:103], v[92:95], a[52:55]
	v_mfma_f32_16x16x32_f16 a[56:59], v[104:107], v[92:95], a[56:59]
	v_mfma_f32_16x16x32_f16 a[60:63], v[108:111], v[92:95], a[60:63]
	s_waitcnt lgkmcnt(0)
	v_mfma_f32_16x16x32_f16 a[0:3], v[128:131], v[112:115], a[0:3]
	v_mfma_f32_16x16x32_f16 a[4:7], v[132:135], v[112:115], a[4:7]
	v_mfma_f32_16x16x32_f16 a[8:11], v[136:139], v[112:115], a[8:11]
	v_mfma_f32_16x16x32_f16 a[12:15], v[140:143], v[112:115], a[12:15]
	v_mfma_f32_16x16x32_f16 a[16:19], v[128:131], v[116:119], a[16:19]
	v_mfma_f32_16x16x32_f16 a[20:23], v[132:135], v[116:119], a[20:23]
	v_mfma_f32_16x16x32_f16 a[24:27], v[136:139], v[116:119], a[24:27]
	v_mfma_f32_16x16x32_f16 a[28:31], v[140:143], v[116:119], a[28:31]
	v_mfma_f32_16x16x32_f16 a[32:35], v[128:131], v[120:123], a[32:35]
	v_mfma_f32_16x16x32_f16 a[36:39], v[132:135], v[120:123], a[36:39]
	v_mfma_f32_16x16x32_f16 a[40:43], v[136:139], v[120:123], a[40:43]
	v_mfma_f32_16x16x32_f16 a[44:47], v[140:143], v[120:123], a[44:47]
	v_mfma_f32_16x16x32_f16 a[48:51], v[128:131], v[124:127], a[48:51]
	v_mfma_f32_16x16x32_f16 a[52:55], v[132:135], v[124:127], a[52:55]
	v_mfma_f32_16x16x32_f16 a[56:59], v[136:139], v[124:127], a[56:59]
	v_mfma_f32_16x16x32_f16 a[60:63], v[140:143], v[124:127], a[60:63]
	s_nop 1
